# barrier top-generation spin + removal of 87 in-place canonicalizing v_max in topk sorting networks
# speedup vs baseline: 1.0040x; 1.0011x over previous
; #define LAS __attribute__((address_space(3)))
; __device__ __forceinline__ void ph_topk(const Frame& F, int layer) {
;     ...
;         for (int p = 0; p < 2; ++p) {
;             const v4u (&qf)[4] = qfa[p];
;             float lo[16], hi[16];
; #pragma unroll
;             for (int kt = 0; kt < 8; ++kt) {
;                 f32x4 acc = (f32x4){0.f, 0.f, 0.f, 0.f};
;                 const LAS unsigned char* kr = lds + TK_SK_OFF + (p * 128 + 16 * kt + l15) * TK_ROW + 16 * g;
; #pragma unroll
;                 for (int st = 0; st < 4; ++st) acc = __builtin_amdgcn_mfma_f32_16x16x32_bf16(*(const LAS bf16x8*)(kr + 64 * st), __builtin_bit_cast(bf16x8, qf[st]), acc, 0, 0, 0);
; #pragma unroll
;                 for (int i = 0; i < 4; ++i) { const float pv = packlow(acc[i], (unsigned)(16 * kt + 4 * g + i), 0x7Fu); if (kt < 4) lo[4 * kt + i] = pv; else hi[4 * (kt - 4) + i] = pv; }
;             }
;             sort16_desc(lo); sort16_desc(hi);
.LBB0_1310:
	ds_read_b128 v[120:123], v60
	ds_read_b128 v[124:127], v60 offset:64
	s_add_i32 s44, s44, s45
	s_cmpk_gt_i32 s44, 0x3ff
	s_cselect_b64 s[14:15], -1, 0
	s_and_b64 vcc, exec, s[14:15]
	s_waitcnt vmcnt(7) lgkmcnt(1)
	v_mfma_f32_16x16x32_bf16 v[120:123], v[120:123], v[2:5], 0
	ds_read_b128 v[128:131], v60 offset:4416
	ds_read_b128 v[170:173], v60 offset:43584
	s_waitcnt vmcnt(6) lgkmcnt(2)
	v_mfma_f32_16x16x32_bf16 v[120:123], v[124:127], v[6:9], v[120:123]
	ds_read_b128 v[124:127], v60 offset:128
	s_waitcnt vmcnt(5) lgkmcnt(0)
	v_mfma_f32_16x16x32_bf16 v[120:123], v[124:127], v[10:13], v[120:123]
	ds_read_b128 v[124:127], v60 offset:192
	s_waitcnt vmcnt(4) lgkmcnt(0)
	v_mfma_f32_16x16x32_bf16 v[122:125], v[124:127], v[14:17], v[120:123]
	s_nop 7
	v_and_or_b32 v119, v124, s59, v62
	v_and_or_b32 v120, v125, s59, v63
	ds_read_b128 v[124:127], v60 offset:4352
	s_waitcnt lgkmcnt(0)
	v_mfma_f32_16x16x32_bf16 v[124:127], v[124:127], v[2:5], 0
	v_and_or_b32 v121, v122, s59, v36
	v_and_or_b32 v122, v123, s59, v61
	v_max_f32_e32 v122, v122, v122
	v_mfma_f32_16x16x32_bf16 v[124:127], v[128:131], v[6:9], v[124:127]
	ds_read_b128 v[128:131], v60 offset:4480
	v_max_f32_e32 v121, v121, v121
	v_max_f32_e32 v119, v119, v119
	s_waitcnt lgkmcnt(0)
	v_mfma_f32_16x16x32_bf16 v[124:127], v[128:131], v[10:13], v[124:127]
	ds_read_b128 v[128:131], v60 offset:4544
	v_max_f32_e32 v120, v120, v120
	s_waitcnt lgkmcnt(0)
	v_mfma_f32_16x16x32_bf16 v[124:127], v[128:131], v[14:17], v[124:127]
	ds_read_b128 v[128:131], v60 offset:8768
	s_nop 6
	v_and_or_b32 v123, v124, s59, v64
	v_and_or_b32 v132, v125, s59, v65
	v_and_or_b32 v133, v126, s59, v66
	v_and_or_b32 v134, v127, s59, v67
	ds_read_b128 v[124:127], v60 offset:8704
	s_waitcnt lgkmcnt(0)
	v_mfma_f32_16x16x32_bf16 v[124:127], v[124:127], v[2:5], 0
	v_max_f32_e32 v123, v123, v123
	v_mfma_f32_16x16x32_bf16 v[124:127], v[128:131], v[6:9], v[124:127]
	ds_read_b128 v[128:131], v60 offset:8832
	s_waitcnt lgkmcnt(0)
	v_mfma_f32_16x16x32_bf16 v[124:127], v[128:131], v[10:13], v[124:127]
	ds_read_b128 v[128:131], v60 offset:8896
	s_waitcnt lgkmcnt(0)
	v_mfma_f32_16x16x32_bf16 v[124:127], v[128:131], v[14:17], v[124:127]
	ds_read_b128 v[128:131], v60 offset:13120
	s_nop 6
	v_and_or_b32 v135, v124, s59, v68
	v_and_or_b32 v136, v125, s59, v69
	v_and_or_b32 v137, v126, s59, v70
	v_and_or_b32 v138, v127, s59, v71
	ds_read_b128 v[124:127], v60 offset:13056
	s_waitcnt lgkmcnt(0)
	v_mfma_f32_16x16x32_bf16 v[124:127], v[124:127], v[2:5], 0
	v_mfma_f32_16x16x32_bf16 v[124:127], v[128:131], v[6:9], v[124:127]
	ds_read_b128 v[128:131], v60 offset:13184
	s_waitcnt lgkmcnt(0)
	v_mfma_f32_16x16x32_bf16 v[124:127], v[128:131], v[10:13], v[124:127]
	ds_read_b128 v[128:131], v60 offset:13248
	s_waitcnt lgkmcnt(0)
	v_mfma_f32_16x16x32_bf16 v[124:127], v[128:131], v[14:17], v[124:127]
	ds_read_b128 v[128:131], v60 offset:17472
	s_nop 6
	v_and_or_b32 v139, v124, s59, v72
	v_and_or_b32 v140, v125, s59, v73
	v_and_or_b32 v141, v126, s59, v74
	v_and_or_b32 v142, v127, s59, v75
	ds_read_b128 v[124:127], v60 offset:17408
	s_waitcnt lgkmcnt(0)
	v_mfma_f32_16x16x32_bf16 v[124:127], v[124:127], v[2:5], 0
	v_mfma_f32_16x16x32_bf16 v[124:127], v[128:131], v[6:9], v[124:127]
	ds_read_b128 v[128:131], v60 offset:17536
	s_waitcnt lgkmcnt(0)
	v_mfma_f32_16x16x32_bf16 v[124:127], v[128:131], v[10:13], v[124:127]
	ds_read_b128 v[128:131], v60 offset:17600
	s_waitcnt lgkmcnt(0)
	v_mfma_f32_16x16x32_bf16 v[124:127], v[128:131], v[14:17], v[124:127]
	ds_read_b128 v[128:131], v60 offset:21824
	s_nop 6
	v_and_or_b32 v143, v124, s59, v76
	v_and_or_b32 v144, v125, s59, v77
	v_and_or_b32 v145, v126, s59, v78
	v_and_or_b32 v146, v127, s59, v79
	ds_read_b128 v[124:127], v60 offset:21760
	s_waitcnt lgkmcnt(0)
	v_mfma_f32_16x16x32_bf16 v[124:127], v[124:127], v[2:5], 0
	v_max_f32_e32 v144, v144, v144
	v_max_f32_e32 v143, v143, v143
	v_max_f32_e32 v159, v143, v144
	v_mfma_f32_16x16x32_bf16 v[124:127], v[128:131], v[6:9], v[124:127]
	ds_read_b128 v[128:131], v60 offset:21888
	v_min_f32_e32 v143, v143, v144
	v_max_f32_e32 v144, v145, v145
	s_waitcnt lgkmcnt(0)
	v_mfma_f32_16x16x32_bf16 v[124:127], v[128:131], v[10:13], v[124:127]
	ds_read_b128 v[128:131], v60 offset:21952
	v_max_f32_e32 v145, v146, v146
	v_max_f32_e32 v146, v145, v144
	s_waitcnt lgkmcnt(0)
	v_mfma_f32_16x16x32_bf16 v[124:127], v[128:131], v[14:17], v[124:127]
	ds_read_b128 v[128:131], v60 offset:26176
	v_min_f32_e32 v144, v145, v144
	s_nop 5
	v_and_or_b32 v147, v124, s59, v80
	v_and_or_b32 v148, v125, s59, v81
	v_and_or_b32 v149, v126, s59, v82
	v_and_or_b32 v150, v127, s59, v83
	ds_read_b128 v[124:127], v60 offset:26112
	s_waitcnt lgkmcnt(0)
	v_mfma_f32_16x16x32_bf16 v[124:127], v[124:127], v[2:5], 0
	v_max_f32_e32 v145, v148, v148
	v_max_f32_e32 v147, v147, v147
	v_max_f32_e32 v148, v147, v145
	v_mfma_f32_16x16x32_bf16 v[124:127], v[128:131], v[6:9], v[124:127]
	ds_read_b128 v[128:131], v60 offset:26240
	v_min_f32_e32 v145, v147, v145
	v_max_f32_e32 v147, v149, v149
	s_waitcnt lgkmcnt(0)
	v_mfma_f32_16x16x32_bf16 v[124:127], v[128:131], v[10:13], v[124:127]
	ds_read_b128 v[128:131], v60 offset:26304
	v_max_f32_e32 v149, v150, v150
	v_max_f32_e32 v150, v149, v147
	s_waitcnt lgkmcnt(0)
	v_mfma_f32_16x16x32_bf16 v[124:127], v[128:131], v[14:17], v[124:127]
	ds_read_b128 v[128:131], v60 offset:30528
	v_min_f32_e32 v147, v149, v147
	s_nop 5
	v_and_or_b32 v151, v124, s59, v84
	v_and_or_b32 v152, v125, s59, v85
	v_and_or_b32 v153, v126, s59, v86
	v_and_or_b32 v154, v127, s59, v87
	ds_read_b128 v[124:127], v60 offset:30464
	s_waitcnt lgkmcnt(0)
; #define LAS __attribute__((address_space(3)))
; __device__ __forceinline__ void ce_desc(float& a, float& b) { const float mx = __builtin_fmaxf(a, b), mn = __builtin_fminf(a, b); a = mx; b = mn; }
; __device__ __forceinline__ void sort16_desc(float (&a)[16]) {
; #pragma unroll
;     for (int k = 2; k <= 16; k <<= 1)
; #pragma unroll
;         for (int j = k >> 1; j > 0; j >>= 1)
; #pragma unroll
;             for (int i = 0; i < 16; ++i) { const int l = i ^ j; if (l > i) { if ((i & k) == 0 || k == 16) ce_desc(a[i], a[l]); else ce_desc(a[l], a[i]); } }
; }
; __device__ __forceinline__ void ph_topk(const Frame& F, int layer) {
;     ...
;             for (int kt = 0; kt < 8; ++kt) {
;                 f32x4 acc = (f32x4){0.f, 0.f, 0.f, 0.f};
;                 const LAS unsigned char* kr = lds + TK_SK_OFF + (p * 128 + 16 * kt + l15) * TK_ROW + 16 * g;
; #pragma unroll
;                 for (int st = 0; st < 4; ++st) acc = __builtin_amdgcn_mfma_f32_16x16x32_bf16(*(const LAS bf16x8*)(kr + 64 * st), __builtin_bit_cast(bf16x8, qf[st]), acc, 0, 0, 0);
; #pragma unroll
;                 for (int i = 0; i < 4; ++i) { const float pv = packlow(acc[i], (unsigned)(16 * kt + 4 * g + i), 0x7Fu); if (kt < 4) lo[4 * kt + i] = pv; else hi[4 * (kt - 4) + i] = pv; }
;             }
;             sort16_desc(lo); sort16_desc(hi);
	v_mfma_f32_16x16x32_bf16 v[124:127], v[124:127], v[2:5], 0
	v_max_f32_e32 v149, v152, v152
	v_max_f32_e32 v151, v151, v151
	v_max_f32_e32 v152, v151, v149
	v_mfma_f32_16x16x32_bf16 v[124:127], v[128:131], v[6:9], v[124:127]
	ds_read_b128 v[128:131], v60 offset:30592
	v_min_f32_e32 v149, v151, v149
	v_max_f32_e32 v151, v153, v153
	s_waitcnt lgkmcnt(0)
	v_mfma_f32_16x16x32_bf16 v[124:127], v[128:131], v[10:13], v[124:127]
	ds_read_b128 v[128:131], v60 offset:30656
	v_max_f32_e32 v153, v154, v154
	v_max_f32_e32 v154, v153, v151
	s_waitcnt lgkmcnt(0)
	v_mfma_f32_16x16x32_bf16 v[124:127], v[128:131], v[14:17], v[124:127]
	v_max_f32_e32 v128, v121, v122
	v_min_f32_e32 v121, v121, v122
	v_max_f32_e32 v122, v120, v119
	v_min_f32_e32 v119, v120, v119
	v_max_f32_e32 v120, v132, v132
	v_max_f32_e32 v129, v123, v120
	v_min_f32_e32 v120, v123, v120
	v_max_f32_e32 v123, v133, v133
	v_max_f32_e32 v130, v134, v134
	v_max_f32_e32 v131, v130, v123
	v_min_f32_e32 v123, v130, v123
	v_max_f32_e32 v130, v136, v136
	v_max_f32_e32 v132, v135, v135
	v_and_or_b32 v124, v124, s59, v88
	v_and_or_b32 v125, v125, s59, v89
	v_max_f32_e32 v133, v132, v130
	v_min_f32_e32 v130, v132, v130
	v_max_f32_e32 v132, v137, v137
	v_max_f32_e32 v134, v138, v138
	v_and_or_b32 v126, v126, s59, v90
	v_and_or_b32 v127, v127, s59, v91
	v_max_f32_e32 v135, v134, v132
	v_min_f32_e32 v132, v134, v132
	v_max_f32_e32 v134, v140, v140
	v_max_f32_e32 v136, v139, v139
	v_max_f32_e32 v137, v136, v134
	v_min_f32_e32 v134, v136, v134
	v_max_f32_e32 v136, v141, v141
	v_max_f32_e32 v138, v142, v142
	v_min_f32_e32 v151, v153, v151
	v_max_f32_e32 v153, v124, v125
	v_min_f32_e32 v124, v124, v125
	v_max_f32_e32 v125, v126, v126
	v_max_f32_e32 v126, v127, v127
	v_max_f32_e32 v139, v138, v136
	v_min_f32_e32 v136, v138, v136
	v_max_f32_e32 v127, v126, v125
	v_min_f32_e32 v125, v126, v125
	v_max_f32_e32 v138, v128, v119
	v_min_f32_e32 v119, v128, v119
	v_max_f32_e32 v128, v121, v122
	v_min_f32_e32 v121, v121, v122
	v_max_f32_e32 v122, v123, v129
	v_min_f32_e32 v123, v123, v129
	v_max_f32_e32 v129, v131, v120
	v_min_f32_e32 v120, v131, v120
	v_max_f32_e32 v131, v133, v132
	v_min_f32_e32 v132, v133, v132
	v_max_f32_e32 v133, v130, v135
	v_min_f32_e32 v130, v130, v135
	v_max_f32_e32 v135, v136, v137
	v_min_f32_e32 v136, v136, v137
	v_max_f32_e32 v137, v139, v134
	v_min_f32_e32 v134, v139, v134
	v_max_f32_e32 v126, v159, v144
	v_min_f32_e32 v144, v159, v144
	v_max_f32_e32 v159, v143, v146
	v_min_f32_e32 v143, v143, v146
	v_max_f32_e32 v146, v147, v148
	v_min_f32_e32 v147, v147, v148
	v_max_f32_e32 v148, v150, v145
	v_min_f32_e32 v145, v150, v145
	v_max_f32_e32 v150, v152, v151
	v_min_f32_e32 v151, v152, v151
	v_max_f32_e32 v152, v149, v154
	v_min_f32_e32 v149, v149, v154
	v_max_f32_e32 v154, v125, v153
	v_min_f32_e32 v125, v125, v153
	v_max_f32_e32 v153, v127, v124
	v_min_f32_e32 v124, v127, v124
	v_max_f32_e32 v139, v138, v128
	v_min_f32_e32 v128, v138, v128
	v_max_f32_e32 v138, v119, v121
	v_min_f32_e32 v119, v119, v121
	v_max_f32_e32 v121, v120, v123
	v_min_f32_e32 v120, v120, v123
	v_max_f32_e32 v123, v129, v122
	v_min_f32_e32 v122, v129, v122
	v_max_f32_e32 v129, v131, v133
	v_min_f32_e32 v131, v131, v133
	v_max_f32_e32 v133, v132, v130
	v_min_f32_e32 v130, v132, v130
	v_max_f32_e32 v132, v134, v136
	v_min_f32_e32 v134, v134, v136
	v_max_f32_e32 v136, v137, v135
	v_min_f32_e32 v135, v137, v135
	v_max_f32_e32 v127, v126, v159
	v_min_f32_e32 v126, v126, v159
	v_max_f32_e32 v159, v144, v143
	v_min_f32_e32 v143, v144, v143
	v_max_f32_e32 v144, v145, v147
	v_min_f32_e32 v145, v145, v147
	v_max_f32_e32 v147, v148, v146
	v_min_f32_e32 v146, v148, v146
	v_max_f32_e32 v148, v150, v152
	v_min_f32_e32 v150, v150, v152
	v_max_f32_e32 v152, v151, v149
	v_min_f32_e32 v149, v151, v149
	v_max_f32_e32 v151, v124, v125
	v_min_f32_e32 v124, v124, v125
	v_max_f32_e32 v125, v153, v154
	v_min_f32_e32 v153, v153, v154
	v_max_f32_e32 v137, v139, v120
	v_min_f32_e32 v120, v139, v120
	v_max_f32_e32 v139, v128, v121
	v_min_f32_e32 v121, v128, v121
	v_max_f32_e32 v128, v138, v122
	v_min_f32_e32 v122, v138, v122
	v_max_f32_e32 v138, v119, v123
	v_min_f32_e32 v119, v119, v123
	v_max_f32_e32 v123, v134, v129
	v_min_f32_e32 v129, v134, v129
	v_max_f32_e32 v134, v132, v131
	v_min_f32_e32 v131, v132, v131
	v_max_f32_e32 v132, v135, v133
	v_min_f32_e32 v133, v135, v133
	v_max_f32_e32 v135, v136, v130
	v_min_f32_e32 v130, v136, v130
	v_max_f32_e32 v154, v127, v145
	v_min_f32_e32 v127, v127, v145
	v_max_f32_e32 v145, v126, v144
	v_min_f32_e32 v126, v126, v144
	v_max_f32_e32 v144, v159, v146
	v_min_f32_e32 v146, v159, v146
	v_max_f32_e32 v159, v143, v147
	v_min_f32_e32 v143, v143, v147
	v_max_f32_e32 v147, v124, v148
	v_min_f32_e32 v124, v124, v148
	v_max_f32_e32 v148, v151, v150
	v_min_f32_e32 v150, v151, v150
	v_max_f32_e32 v151, v153, v152
	v_min_f32_e32 v152, v153, v152
	v_max_f32_e32 v153, v125, v149
	v_min_f32_e32 v125, v125, v149
	v_max_f32_e32 v136, v137, v128
	v_min_f32_e32 v128, v137, v128
	v_max_f32_e32 v137, v139, v138
	v_min_f32_e32 v138, v139, v138
	v_max_f32_e32 v139, v120, v122
	v_min_f32_e32 v120, v120, v122
	v_max_f32_e32 v122, v121, v119
	v_min_f32_e32 v119, v121, v119
	v_max_f32_e32 v121, v133, v129
	v_min_f32_e32 v129, v133, v129
	v_max_f32_e32 v133, v130, v131
	v_min_f32_e32 v130, v130, v131
	v_max_f32_e32 v131, v132, v123
	v_min_f32_e32 v123, v132, v123
	v_max_f32_e32 v132, v135, v134
	v_min_f32_e32 v134, v135, v134
	v_max_f32_e32 v149, v154, v144
	v_min_f32_e32 v144, v154, v144
	v_max_f32_e32 v154, v145, v159
	v_min_f32_e32 v145, v145, v159
	v_max_f32_e32 v159, v127, v146
	v_min_f32_e32 v127, v127, v146
; __device__ __forceinline__ void ce_desc(float& a, float& b) { const float mx = __builtin_fmaxf(a, b), mn = __builtin_fminf(a, b); a = mx; b = mn; }
; __device__ __forceinline__ void sort16_desc(float (&a)[16]) {
; #pragma unroll
;     for (int k = 2; k <= 16; k <<= 1)
; #pragma unroll
;         for (int j = k >> 1; j > 0; j >>= 1)
; #pragma unroll
;             for (int i = 0; i < 16; ++i) { const int l = i ^ j; if (l > i) { if ((i & k) == 0 || k == 16) ce_desc(a[i], a[l]); else ce_desc(a[l], a[i]); } }
; }
; __device__ __forceinline__ void bitonic_merge16_desc(float (&a)[16]) {
; #pragma unroll
;     for (int j = 8; j > 0; j >>= 1)
; #pragma unroll
;         for (int i = 0; i < 16; ++i) { const int l = i ^ j; if (l > i) ce_desc(a[i], a[l]); }
; }
; __device__ __forceinline__ void ph_topk(const Frame& F, int layer) {
;     ...
;             sort16_desc(lo); sort16_desc(hi);
; #pragma unroll
;             for (int i = 0; i < 16; ++i) lo[i] = __builtin_fmaxf(lo[i], hi[15 - i]);
;             bitonic_merge16_desc(lo);
	v_max_f32_e32 v146, v126, v143
	v_min_f32_e32 v126, v126, v143
	v_max_f32_e32 v143, v152, v124
	v_min_f32_e32 v124, v152, v124
	v_max_f32_e32 v152, v125, v150
	v_min_f32_e32 v125, v125, v150
	v_max_f32_e32 v150, v151, v147
	v_min_f32_e32 v147, v151, v147
	v_max_f32_e32 v151, v153, v148
	v_min_f32_e32 v148, v153, v148
	v_max_f32_e32 v135, v136, v137
	v_min_f32_e32 v136, v136, v137
	v_max_f32_e32 v137, v128, v138
	v_min_f32_e32 v128, v128, v138
	v_max_f32_e32 v138, v139, v122
	v_min_f32_e32 v122, v139, v122
	v_max_f32_e32 v139, v120, v119
	v_min_f32_e32 v119, v120, v119
	v_max_f32_e32 v120, v130, v129
	v_min_f32_e32 v129, v130, v129
	v_max_f32_e32 v130, v133, v121
	v_min_f32_e32 v121, v133, v121
	v_max_f32_e32 v133, v134, v123
	v_min_f32_e32 v123, v134, v123
	v_max_f32_e32 v134, v132, v131
	v_min_f32_e32 v131, v132, v131
	v_max_f32_e32 v153, v149, v154
	v_min_f32_e32 v149, v149, v154
	v_max_f32_e32 v154, v144, v145
	v_min_f32_e32 v144, v144, v145
	v_max_f32_e32 v145, v159, v146
	v_min_f32_e32 v146, v159, v146
	v_max_f32_e32 v159, v127, v126
	v_min_f32_e32 v126, v127, v126
	v_max_f32_e32 v127, v125, v124
	v_min_f32_e32 v124, v125, v124
	v_max_f32_e32 v125, v152, v143
	v_min_f32_e32 v143, v152, v143
	v_max_f32_e32 v152, v148, v147
	v_min_f32_e32 v147, v148, v147
	v_max_f32_e32 v148, v151, v150
	v_min_f32_e32 v150, v151, v150
	v_max_f32_e32 v132, v135, v129
	v_min_f32_e32 v129, v135, v129
	v_max_f32_e32 v135, v136, v120
	v_min_f32_e32 v120, v136, v120
	v_max_f32_e32 v136, v137, v121
	v_min_f32_e32 v121, v137, v121
	v_max_f32_e32 v137, v128, v130
	v_min_f32_e32 v128, v128, v130
	v_max_f32_e32 v130, v138, v123
	v_min_f32_e32 v123, v138, v123
	v_max_f32_e32 v138, v122, v133
	v_min_f32_e32 v122, v122, v133
	v_max_f32_e32 v133, v139, v131
	v_min_f32_e32 v131, v139, v131
	v_max_f32_e32 v139, v119, v134
	v_min_f32_e32 v119, v119, v134
	v_max_f32_e32 v151, v153, v124
	v_min_f32_e32 v124, v153, v124
	v_max_f32_e32 v153, v149, v127
	v_min_f32_e32 v127, v149, v127
	v_max_f32_e32 v149, v154, v143
	v_min_f32_e32 v143, v154, v143
	v_max_f32_e32 v154, v144, v125
	v_min_f32_e32 v125, v144, v125
	v_max_f32_e32 v144, v145, v147
	v_min_f32_e32 v145, v145, v147
	v_max_f32_e32 v147, v146, v152
	v_min_f32_e32 v146, v146, v152
	v_max_f32_e32 v152, v159, v150
	v_min_f32_e32 v150, v159, v150
	v_max_f32_e32 v159, v126, v148
	v_min_f32_e32 v126, v126, v148
	v_max_f32_e32 v134, v132, v130
	v_min_f32_e32 v130, v132, v130
	v_max_f32_e32 v132, v135, v138
	v_min_f32_e32 v135, v135, v138
	v_max_f32_e32 v138, v136, v133
	v_min_f32_e32 v133, v136, v133
	v_max_f32_e32 v136, v137, v139
	v_min_f32_e32 v137, v137, v139
	v_max_f32_e32 v139, v129, v123
	v_min_f32_e32 v123, v129, v123
	v_max_f32_e32 v129, v120, v122
	v_min_f32_e32 v120, v120, v122
	v_max_f32_e32 v122, v121, v131
	v_min_f32_e32 v121, v121, v131
	v_max_f32_e32 v131, v128, v119
	v_min_f32_e32 v119, v128, v119
	v_max_f32_e32 v148, v151, v144
	v_min_f32_e32 v144, v151, v144
	v_max_f32_e32 v151, v153, v147
	v_min_f32_e32 v147, v153, v147
	v_max_f32_e32 v153, v149, v152
	v_min_f32_e32 v149, v149, v152
	v_max_f32_e32 v152, v154, v159
	v_min_f32_e32 v154, v154, v159
	v_max_f32_e32 v159, v124, v145
	v_min_f32_e32 v124, v124, v145
	v_max_f32_e32 v145, v127, v146
	v_min_f32_e32 v127, v127, v146
	v_max_f32_e32 v146, v143, v150
	v_min_f32_e32 v143, v143, v150
	v_max_f32_e32 v150, v125, v126
	v_min_f32_e32 v125, v125, v126
	v_max_f32_e32 v128, v134, v138
	v_min_f32_e32 v134, v134, v138
	v_max_f32_e32 v138, v132, v136
	v_min_f32_e32 v132, v132, v136
	v_max_f32_e32 v136, v130, v133
	v_min_f32_e32 v130, v130, v133
	v_max_f32_e32 v133, v135, v137
	v_min_f32_e32 v135, v135, v137
	v_max_f32_e32 v137, v139, v122
	v_min_f32_e32 v122, v139, v122
	v_max_f32_e32 v139, v129, v131
	v_min_f32_e32 v129, v129, v131
	v_max_f32_e32 v131, v123, v121
	v_min_f32_e32 v121, v123, v121
	v_max_f32_e32 v123, v120, v119
	v_min_f32_e32 v119, v120, v119
	v_max_f32_e32 v126, v148, v153
	v_min_f32_e32 v148, v148, v153
	v_max_f32_e32 v153, v151, v152
	v_min_f32_e32 v151, v151, v152
	v_max_f32_e32 v152, v144, v149
	v_min_f32_e32 v144, v144, v149
	v_max_f32_e32 v149, v147, v154
	v_min_f32_e32 v147, v147, v154
	v_max_f32_e32 v154, v159, v146
	v_min_f32_e32 v146, v159, v146
	v_max_f32_e32 v159, v145, v150
	v_min_f32_e32 v145, v145, v150
	v_max_f32_e32 v150, v124, v143
	v_min_f32_e32 v124, v124, v143
	v_max_f32_e32 v143, v127, v125
	v_min_f32_e32 v120, v128, v138
	v_min_f32_e32 v142, v130, v135
	v_min_f32_e32 v155, v137, v139
	v_min_f32_e32 v156, v122, v129
	v_min_f32_e32 v158, v121, v119
	v_min_f32_e32 v125, v127, v125
	v_min_f32_e32 v127, v126, v153
	v_min_f32_e32 v161, v152, v149
	v_min_f32_e32 v165, v146, v145
	v_min_f32_e32 v166, v150, v143
	v_min_f32_e32 v140, v134, v132
	v_min_f32_e32 v141, v136, v133
	v_min_f32_e32 v164, v154, v159
	v_min_f32_e32 v167, v124, v125
	v_max3_f32 v120, v120, v124, v125
	v_max3_f32 v124, v134, v132, v166
	v_max3_f32 v132, v136, v133, v165
	v_max3_f32 v134, v142, v154, v159
	v_max3_f32 v136, v155, v144, v147
	v_max3_f32 v122, v122, v129, v161
	v_max3_f32 v129, v156, v152, v149
	v_max3_f32 v119, v121, v119, v127
	v_max3_f32 v121, v158, v126, v153
	ds_read_b128 v[152:155], v60 offset:34816
	v_min_f32_e32 v157, v131, v123
	v_min_f32_e32 v160, v148, v151
	v_max3_f32 v123, v131, v123, v160
	v_max3_f32 v131, v157, v148, v151
	ds_read_b128 v[156:159], v60 offset:34880
	s_waitcnt vmcnt(3) lgkmcnt(1)
	v_mfma_f32_16x16x32_bf16 v[152:155], v[152:155], v[18:21], 0
	v_max3_f32 v128, v128, v138, v167
	v_max3_f32 v130, v130, v135, v164
	ds_read_b128 v[164:167], v60 offset:39232
	s_waitcnt vmcnt(2) lgkmcnt(1)
; #define LAS __attribute__((address_space(3)))
; __device__ __forceinline__ void ph_topk(const Frame& F, int layer) {
;     ...
;         for (int p = 0; p < 2; ++p) {
;             const v4u (&qf)[4] = qfa[p];
;             float lo[16], hi[16];
; #pragma unroll
;             for (int kt = 0; kt < 8; ++kt) {
;                 f32x4 acc = (f32x4){0.f, 0.f, 0.f, 0.f};
;                 const LAS unsigned char* kr = lds + TK_SK_OFF + (p * 128 + 16 * kt + l15) * TK_ROW + 16 * g;
; #pragma unroll
;                 for (int st = 0; st < 4; ++st) acc = __builtin_amdgcn_mfma_f32_16x16x32_bf16(*(const LAS bf16x8*)(kr + 64 * st), __builtin_bit_cast(bf16x8, qf[st]), acc, 0, 0, 0);
; #pragma unroll
;                 for (int i = 0; i < 4; ++i) { const float pv = packlow(acc[i], (unsigned)(16 * kt + 4 * g + i), 0x7Fu); if (kt < 4) lo[4 * kt + i] = pv; else hi[4 * (kt - 4) + i] = pv; }
;             }
;             sort16_desc(lo); sort16_desc(hi);
; #pragma unroll
;             for (int i = 0; i < 16; ++i) lo[i] = __builtin_fmaxf(lo[i], hi[15 - i]);
;             bitonic_merge16_desc(lo);
	v_mfma_f32_16x16x32_bf16 v[152:155], v[156:159], v[22:25], v[152:155]
	ds_read_b128 v[156:159], v60 offset:34944
	v_min_f32_e32 v163, v144, v147
	v_max3_f32 v135, v137, v139, v163
	s_waitcnt vmcnt(1) lgkmcnt(0)
	v_mfma_f32_16x16x32_bf16 v[152:155], v[156:159], v[26:29], v[152:155]
	ds_read_b128 v[156:159], v60 offset:35008
	v_max3_f32 v125, v140, v150, v143
	v_max3_f32 v133, v141, v146, v145
	s_waitcnt vmcnt(0) lgkmcnt(0)
	v_mfma_f32_16x16x32_bf16 v[154:157], v[156:159], v[30:33], v[152:155]
	v_max_f32_e32 v126, v128, v135
	v_min_f32_e32 v127, v128, v135
	v_max_f32_e32 v128, v120, v136
	s_nop 4
	v_and_or_b32 v151, v156, s59, v62
	v_and_or_b32 v152, v157, s59, v63
	ds_read_b128 v[156:159], v60 offset:39168
	s_waitcnt lgkmcnt(0)
	v_mfma_f32_16x16x32_bf16 v[156:159], v[156:159], v[18:21], 0
	v_and_or_b32 v153, v154, s59, v36
	v_and_or_b32 v154, v155, s59, v61
	v_max_f32_e32 v154, v154, v154
	v_mfma_f32_16x16x32_bf16 v[156:159], v[164:167], v[22:25], v[156:159]
	ds_read_b128 v[164:167], v60 offset:39296
	v_max_f32_e32 v153, v153, v153
	v_max_f32_e32 v151, v151, v151
	s_waitcnt lgkmcnt(0)
	v_mfma_f32_16x16x32_bf16 v[156:159], v[164:167], v[26:29], v[156:159]
	ds_read_b128 v[164:167], v60 offset:39360
	v_max_f32_e32 v152, v152, v152
	v_min_f32_e32 v120, v120, v136
	s_waitcnt lgkmcnt(0)
	v_mfma_f32_16x16x32_bf16 v[158:161], v[164:167], v[30:33], v[156:159]
	ds_read_b128 v[164:167], v60 offset:43520
	v_max_f32_e32 v135, v124, v122
	v_min_f32_e32 v122, v124, v122
	s_waitcnt lgkmcnt(0)
	v_mfma_f32_16x16x32_bf16 v[164:167], v[164:167], v[18:21], 0
	s_nop 2
	v_and_or_b32 v157, v158, s59, v64
	v_and_or_b32 v158, v159, s59, v65
	v_and_or_b32 v155, v160, s59, v66
	v_mfma_f32_16x16x32_bf16 v[164:167], v[170:173], v[22:25], v[164:167]
	ds_read_b128 v[170:173], v60 offset:43648
	v_and_or_b32 v156, v161, s59, v67
	v_max_f32_e32 v157, v157, v157
	s_waitcnt lgkmcnt(0)
	v_mfma_f32_16x16x32_bf16 v[164:167], v[170:173], v[26:29], v[164:167]
	ds_read_b128 v[170:173], v60 offset:43712
	v_max_f32_e32 v155, v155, v155
	v_max_f32_e32 v156, v156, v156
	s_waitcnt lgkmcnt(0)
	v_mfma_f32_16x16x32_bf16 v[164:167], v[170:173], v[30:33], v[164:167]
	ds_read_b128 v[170:173], v60 offset:47936
	v_max_f32_e32 v124, v125, v129
	v_min_f32_e32 v125, v125, v129
	s_nop 4
	v_and_or_b32 v161, v164, s59, v68
	v_and_or_b32 v163, v165, s59, v69
	v_and_or_b32 v159, v166, s59, v70
	v_and_or_b32 v160, v167, s59, v71
	ds_read_b128 v[164:167], v60 offset:47872
	s_waitcnt lgkmcnt(0)
	v_mfma_f32_16x16x32_bf16 v[164:167], v[164:167], v[18:21], 0
	v_max_f32_e32 v161, v161, v161
	v_max_f32_e32 v159, v159, v159
	v_max_f32_e32 v160, v160, v160
	v_mfma_f32_16x16x32_bf16 v[164:167], v[170:173], v[22:25], v[164:167]
	ds_read_b128 v[170:173], v60 offset:48000
	v_max_f32_e32 v129, v132, v123
	v_min_f32_e32 v123, v132, v123
	s_waitcnt lgkmcnt(0)
	v_mfma_f32_16x16x32_bf16 v[164:167], v[170:173], v[26:29], v[164:167]
	ds_read_b128 v[170:173], v60 offset:48064
	v_max_f32_e32 v132, v133, v131
	v_min_f32_e32 v131, v133, v131
	s_waitcnt lgkmcnt(0)
	v_mfma_f32_16x16x32_bf16 v[164:167], v[170:173], v[30:33], v[164:167]
	ds_read_b128 v[170:173], v60 offset:52288
	v_max_f32_e32 v133, v130, v119
	v_min_f32_e32 v119, v130, v119
	s_nop 4
	v_and_or_b32 v174, v164, s59, v72
	v_and_or_b32 v175, v165, s59, v73
	v_and_or_b32 v176, v166, s59, v74
	v_and_or_b32 v177, v167, s59, v75
	ds_read_b128 v[164:167], v60 offset:52224
	s_waitcnt lgkmcnt(0)
	v_mfma_f32_16x16x32_bf16 v[164:167], v[164:167], v[18:21], 0
	v_max_f32_e32 v130, v134, v121
	v_min_f32_e32 v121, v134, v121
	v_max_f32_e32 v134, v126, v129
	v_mfma_f32_16x16x32_bf16 v[164:167], v[170:173], v[22:25], v[164:167]
	ds_read_b128 v[170:173], v60 offset:52352
	v_min_f32_e32 v126, v126, v129
	v_max_f32_e32 v129, v128, v132
	s_waitcnt lgkmcnt(0)
	v_mfma_f32_16x16x32_bf16 v[164:167], v[170:173], v[26:29], v[164:167]
	ds_read_b128 v[170:173], v60 offset:52416
	v_min_f32_e32 v128, v128, v132
	v_max_f32_e32 v132, v135, v133
	s_waitcnt lgkmcnt(0)
	v_mfma_f32_16x16x32_bf16 v[164:167], v[170:173], v[30:33], v[164:167]
	ds_read_b128 v[170:173], v60 offset:56640
	v_min_f32_e32 v133, v135, v133
	v_max_f32_e32 v135, v124, v130
	s_nop 4
	v_and_or_b32 v178, v164, s59, v76
	v_and_or_b32 v179, v165, s59, v77
	v_and_or_b32 v180, v166, s59, v78
	v_and_or_b32 v181, v167, s59, v79
	ds_read_b128 v[164:167], v60 offset:56576
	s_waitcnt lgkmcnt(0)
	v_mfma_f32_16x16x32_bf16 v[164:167], v[164:167], v[18:21], 0
	v_max_f32_e32 v179, v179, v179
	v_max_f32_e32 v178, v178, v178
	v_max_f32_e32 v194, v178, v179
	v_mfma_f32_16x16x32_bf16 v[164:167], v[170:173], v[22:25], v[164:167]
	ds_read_b128 v[170:173], v60 offset:56704
	v_min_f32_e32 v178, v178, v179
	v_max_f32_e32 v179, v180, v180
	s_waitcnt lgkmcnt(0)
	v_mfma_f32_16x16x32_bf16 v[164:167], v[170:173], v[26:29], v[164:167]
	ds_read_b128 v[170:173], v60 offset:56768
	v_max_f32_e32 v180, v181, v181
	v_max_f32_e32 v181, v180, v179
	s_waitcnt lgkmcnt(0)
	v_mfma_f32_16x16x32_bf16 v[164:167], v[170:173], v[30:33], v[164:167]
	ds_read_b128 v[170:173], v60 offset:60992
	v_min_f32_e32 v179, v180, v179
	v_min_f32_e32 v124, v124, v130
	s_nop 4
	v_and_or_b32 v182, v164, s59, v80
	v_and_or_b32 v183, v165, s59, v81
	v_and_or_b32 v184, v166, s59, v82
	v_and_or_b32 v185, v167, s59, v83
	ds_read_b128 v[164:167], v60 offset:60928
	s_waitcnt lgkmcnt(0)
	v_mfma_f32_16x16x32_bf16 v[164:167], v[164:167], v[18:21], 0
	v_max_f32_e32 v180, v183, v183
	v_max_f32_e32 v182, v182, v182
	v_max_f32_e32 v183, v182, v180
	v_mfma_f32_16x16x32_bf16 v[164:167], v[170:173], v[22:25], v[164:167]
	ds_read_b128 v[170:173], v60 offset:61056
	v_min_f32_e32 v180, v182, v180
	v_max_f32_e32 v182, v184, v184
	s_waitcnt lgkmcnt(0)
; #define LAS __attribute__((address_space(3)))
; __device__ __forceinline__ void ce_desc(float& a, float& b) { const float mx = __builtin_fmaxf(a, b), mn = __builtin_fminf(a, b); a = mx; b = mn; }
; __device__ __forceinline__ void sort16_desc(float (&a)[16]) {
; #pragma unroll
;     for (int k = 2; k <= 16; k <<= 1)
; #pragma unroll
;         for (int j = k >> 1; j > 0; j >>= 1)
; #pragma unroll
;             for (int i = 0; i < 16; ++i) { const int l = i ^ j; if (l > i) { if ((i & k) == 0 || k == 16) ce_desc(a[i], a[l]); else ce_desc(a[l], a[i]); } }
; }
; __device__ __forceinline__ void ph_topk(const Frame& F, int layer) {
;     ...
;             for (int kt = 0; kt < 8; ++kt) {
;                 f32x4 acc = (f32x4){0.f, 0.f, 0.f, 0.f};
;                 const LAS unsigned char* kr = lds + TK_SK_OFF + (p * 128 + 16 * kt + l15) * TK_ROW + 16 * g;
; #pragma unroll
;                 for (int st = 0; st < 4; ++st) acc = __builtin_amdgcn_mfma_f32_16x16x32_bf16(*(const LAS bf16x8*)(kr + 64 * st), __builtin_bit_cast(bf16x8, qf[st]), acc, 0, 0, 0);
; #pragma unroll
;                 for (int i = 0; i < 4; ++i) { const float pv = packlow(acc[i], (unsigned)(16 * kt + 4 * g + i), 0x7Fu); if (kt < 4) lo[4 * kt + i] = pv; else hi[4 * (kt - 4) + i] = pv; }
;             }
;             sort16_desc(lo); sort16_desc(hi);
	v_mfma_f32_16x16x32_bf16 v[164:167], v[170:173], v[26:29], v[164:167]
	ds_read_b128 v[170:173], v60 offset:61120
	v_max_f32_e32 v184, v185, v185
	v_max_f32_e32 v185, v184, v182
	s_waitcnt lgkmcnt(0)
	v_mfma_f32_16x16x32_bf16 v[164:167], v[170:173], v[30:33], v[164:167]
	ds_read_b128 v[170:173], v60 offset:65344
	v_min_f32_e32 v182, v184, v182
	v_max_f32_e32 v130, v127, v123
	s_nop 4
	v_and_or_b32 v186, v164, s59, v84
	v_and_or_b32 v187, v165, s59, v85
	v_and_or_b32 v188, v166, s59, v86
	v_and_or_b32 v189, v167, s59, v87
	ds_read_b128 v[164:167], v60 offset:65280
	s_waitcnt lgkmcnt(0)
	v_mfma_f32_16x16x32_bf16 v[164:167], v[164:167], v[18:21], 0
	v_max_f32_e32 v184, v187, v187
	v_max_f32_e32 v186, v186, v186
	v_max_f32_e32 v187, v186, v184
	v_mfma_f32_16x16x32_bf16 v[164:167], v[170:173], v[22:25], v[164:167]
	ds_read_b128 v[170:173], v60 offset:65408
	v_min_f32_e32 v184, v186, v184
	v_max_f32_e32 v186, v188, v188
	s_waitcnt lgkmcnt(0)
	v_mfma_f32_16x16x32_bf16 v[164:167], v[170:173], v[26:29], v[164:167]
	ds_read_b128 v[170:173], v60 offset:65472
	v_max_f32_e32 v188, v189, v189
	v_max_f32_e32 v189, v188, v186
	s_waitcnt lgkmcnt(0)
	v_mfma_f32_16x16x32_bf16 v[164:167], v[170:173], v[30:33], v[164:167]
	v_max_f32_e32 v170, v153, v154
	v_min_f32_e32 v153, v153, v154
	v_max_f32_e32 v154, v152, v151
	v_min_f32_e32 v151, v152, v151
	v_max_f32_e32 v152, v158, v158
	s_nop 2
	v_and_or_b32 v164, v164, s59, v88
	v_and_or_b32 v165, v165, s59, v89
	v_max_f32_e32 v158, v157, v152
	v_min_f32_e32 v152, v157, v152
	v_max_f32_e32 v157, v156, v155
	v_min_f32_e32 v155, v156, v155
	v_max_f32_e32 v156, v163, v163
	v_and_or_b32 v166, v166, s59, v90
	v_and_or_b32 v167, v167, s59, v91
	v_max_f32_e32 v163, v161, v156
	v_min_f32_e32 v156, v161, v156
	v_max_f32_e32 v161, v160, v159
	v_min_f32_e32 v159, v160, v159
	v_max_f32_e32 v160, v175, v175
	v_max_f32_e32 v171, v174, v174
	v_max_f32_e32 v172, v171, v160
	v_min_f32_e32 v160, v171, v160
	v_max_f32_e32 v171, v176, v176
	v_max_f32_e32 v173, v177, v177
	v_min_f32_e32 v186, v188, v186
	v_max_f32_e32 v188, v164, v165
	v_min_f32_e32 v164, v164, v165
	v_max_f32_e32 v165, v166, v166
	v_max_f32_e32 v166, v167, v167
	v_max_f32_e32 v174, v173, v171
	v_min_f32_e32 v171, v173, v171
	v_max_f32_e32 v167, v166, v165
	v_min_f32_e32 v165, v166, v165
	v_max_f32_e32 v173, v170, v151
	v_min_f32_e32 v151, v170, v151
	v_max_f32_e32 v170, v153, v154
	v_min_f32_e32 v153, v153, v154
	v_max_f32_e32 v154, v155, v158
	v_min_f32_e32 v155, v155, v158
	v_max_f32_e32 v158, v157, v152
	v_min_f32_e32 v152, v157, v152
	v_max_f32_e32 v157, v163, v159
	v_min_f32_e32 v159, v163, v159
	v_max_f32_e32 v163, v156, v161
	v_min_f32_e32 v156, v156, v161
	v_max_f32_e32 v161, v171, v172
	v_min_f32_e32 v171, v171, v172
	v_max_f32_e32 v172, v174, v160
	v_min_f32_e32 v160, v174, v160
	v_max_f32_e32 v166, v194, v179
	v_min_f32_e32 v179, v194, v179
	v_max_f32_e32 v194, v178, v181
	v_min_f32_e32 v178, v178, v181
	v_max_f32_e32 v181, v182, v183
	v_min_f32_e32 v182, v182, v183
	v_max_f32_e32 v183, v185, v180
	v_min_f32_e32 v180, v185, v180
	v_max_f32_e32 v185, v187, v186
	v_min_f32_e32 v186, v187, v186
	v_max_f32_e32 v187, v184, v189
	v_min_f32_e32 v184, v184, v189
	v_max_f32_e32 v189, v165, v188
	v_min_f32_e32 v165, v165, v188
	v_max_f32_e32 v188, v167, v164
	v_min_f32_e32 v164, v167, v164
	v_max_f32_e32 v174, v173, v170
	v_min_f32_e32 v170, v173, v170
	v_max_f32_e32 v173, v151, v153
	v_min_f32_e32 v151, v151, v153
	v_max_f32_e32 v153, v152, v155
	v_min_f32_e32 v152, v152, v155
	v_max_f32_e32 v155, v158, v154
	v_min_f32_e32 v154, v158, v154
	v_max_f32_e32 v158, v157, v163
	v_min_f32_e32 v157, v157, v163
	v_max_f32_e32 v163, v159, v156
	v_min_f32_e32 v156, v159, v156
	v_max_f32_e32 v159, v160, v171
	v_min_f32_e32 v160, v160, v171
	v_max_f32_e32 v171, v172, v161
	v_min_f32_e32 v161, v172, v161
	v_max_f32_e32 v167, v166, v194
	v_min_f32_e32 v166, v166, v194
	v_max_f32_e32 v194, v179, v178
	v_min_f32_e32 v178, v179, v178
	v_max_f32_e32 v179, v180, v182
	v_min_f32_e32 v180, v180, v182
	v_max_f32_e32 v182, v183, v181
	v_min_f32_e32 v181, v183, v181
	v_max_f32_e32 v183, v185, v187
	v_min_f32_e32 v185, v185, v187
	v_max_f32_e32 v187, v186, v184
	v_min_f32_e32 v184, v186, v184
	v_max_f32_e32 v186, v164, v165
	v_min_f32_e32 v164, v164, v165
	v_max_f32_e32 v165, v188, v189
	v_min_f32_e32 v188, v188, v189
	v_max_f32_e32 v172, v174, v152
	v_min_f32_e32 v152, v174, v152
	v_max_f32_e32 v174, v170, v153
	v_min_f32_e32 v153, v170, v153
	v_max_f32_e32 v170, v173, v154
	v_min_f32_e32 v154, v173, v154
	v_max_f32_e32 v173, v151, v155
	v_min_f32_e32 v151, v151, v155
	v_max_f32_e32 v155, v160, v158
	v_min_f32_e32 v158, v160, v158
	v_max_f32_e32 v160, v159, v157
	v_min_f32_e32 v157, v159, v157
	v_max_f32_e32 v159, v161, v163
	v_min_f32_e32 v161, v161, v163
	v_max_f32_e32 v163, v171, v156
	v_min_f32_e32 v156, v171, v156
	v_max_f32_e32 v189, v167, v180
	v_min_f32_e32 v167, v167, v180
	v_max_f32_e32 v180, v166, v179
	v_min_f32_e32 v166, v166, v179
	v_max_f32_e32 v179, v194, v181
	v_min_f32_e32 v181, v194, v181
	v_max_f32_e32 v194, v178, v182
	v_min_f32_e32 v178, v178, v182
	v_max_f32_e32 v182, v164, v183
	v_min_f32_e32 v164, v164, v183
	v_max_f32_e32 v183, v186, v185
	v_min_f32_e32 v185, v186, v185
	v_max_f32_e32 v186, v188, v187
	v_min_f32_e32 v187, v188, v187
	v_max_f32_e32 v188, v165, v184
	v_min_f32_e32 v165, v165, v184
	v_max_f32_e32 v171, v172, v170
	v_min_f32_e32 v170, v172, v170
	v_max_f32_e32 v172, v174, v173
	v_min_f32_e32 v173, v174, v173
	v_max_f32_e32 v174, v152, v154
	v_min_f32_e32 v152, v152, v154
	v_max_f32_e32 v154, v153, v151
	v_min_f32_e32 v151, v153, v151
; __device__ __forceinline__ void ce_desc(float& a, float& b) { const float mx = __builtin_fmaxf(a, b), mn = __builtin_fminf(a, b); a = mx; b = mn; }
; __device__ __forceinline__ void sort16_desc(float (&a)[16]) {
; #pragma unroll
;     for (int k = 2; k <= 16; k <<= 1)
; #pragma unroll
;         for (int j = k >> 1; j > 0; j >>= 1)
; #pragma unroll
;             for (int i = 0; i < 16; ++i) { const int l = i ^ j; if (l > i) { if ((i & k) == 0 || k == 16) ce_desc(a[i], a[l]); else ce_desc(a[l], a[i]); } }
; }
; __device__ __forceinline__ void bitonic_merge16_desc(float (&a)[16]) {
; #pragma unroll
;     for (int j = 8; j > 0; j >>= 1)
; #pragma unroll
;         for (int i = 0; i < 16; ++i) { const int l = i ^ j; if (l > i) ce_desc(a[i], a[l]); }
; }
; __device__ __forceinline__ void ph_topk(const Frame& F, int layer) {
;     ...
;             sort16_desc(lo); sort16_desc(hi);
; #pragma unroll
;             for (int i = 0; i < 16; ++i) lo[i] = __builtin_fmaxf(lo[i], hi[15 - i]);
;             bitonic_merge16_desc(lo);
	v_max_f32_e32 v153, v161, v158
	v_min_f32_e32 v158, v161, v158
	v_max_f32_e32 v161, v156, v157
	v_min_f32_e32 v156, v156, v157
	v_max_f32_e32 v157, v159, v155
	v_min_f32_e32 v155, v159, v155
	v_max_f32_e32 v159, v163, v160
	v_min_f32_e32 v160, v163, v160
	v_max_f32_e32 v184, v189, v179
	v_min_f32_e32 v179, v189, v179
	v_max_f32_e32 v189, v180, v194
	v_min_f32_e32 v180, v180, v194
	v_max_f32_e32 v194, v167, v181
	v_min_f32_e32 v167, v167, v181
	v_max_f32_e32 v181, v166, v178
	v_min_f32_e32 v166, v166, v178
	v_max_f32_e32 v178, v187, v164
	v_min_f32_e32 v164, v187, v164
	v_max_f32_e32 v187, v165, v185
	v_min_f32_e32 v165, v165, v185
	v_max_f32_e32 v185, v186, v182
	v_min_f32_e32 v182, v186, v182
	v_max_f32_e32 v186, v188, v183
	v_min_f32_e32 v183, v188, v183
	v_max_f32_e32 v163, v171, v172
	v_min_f32_e32 v171, v171, v172
	v_max_f32_e32 v172, v170, v173
	v_min_f32_e32 v170, v170, v173
	v_max_f32_e32 v173, v174, v154
	v_min_f32_e32 v154, v174, v154
	v_max_f32_e32 v174, v152, v151
	v_min_f32_e32 v151, v152, v151
	v_max_f32_e32 v152, v156, v158
	v_min_f32_e32 v156, v156, v158
	v_max_f32_e32 v158, v161, v153
	v_min_f32_e32 v153, v161, v153
	v_max_f32_e32 v161, v160, v155
	v_min_f32_e32 v155, v160, v155
	v_max_f32_e32 v160, v159, v157
	v_min_f32_e32 v157, v159, v157
	v_max_f32_e32 v188, v184, v189
	v_min_f32_e32 v184, v184, v189
	v_max_f32_e32 v189, v179, v180
	v_min_f32_e32 v179, v179, v180
	v_max_f32_e32 v180, v194, v181
	v_min_f32_e32 v181, v194, v181
	v_max_f32_e32 v194, v167, v166
	v_min_f32_e32 v166, v167, v166
	v_max_f32_e32 v167, v165, v164
	v_min_f32_e32 v164, v165, v164
	v_max_f32_e32 v165, v187, v178
	v_min_f32_e32 v178, v187, v178
	v_max_f32_e32 v187, v183, v182
	v_min_f32_e32 v182, v183, v182
	v_max_f32_e32 v183, v186, v185
	v_min_f32_e32 v185, v186, v185
	v_max_f32_e32 v159, v163, v156
	v_min_f32_e32 v156, v163, v156
	v_max_f32_e32 v163, v171, v152
	v_min_f32_e32 v152, v171, v152
	v_max_f32_e32 v171, v172, v153
	v_min_f32_e32 v153, v172, v153
	v_max_f32_e32 v172, v170, v158
	v_min_f32_e32 v158, v170, v158
	v_max_f32_e32 v170, v173, v155
	v_min_f32_e32 v155, v173, v155
	v_max_f32_e32 v173, v154, v161
	v_min_f32_e32 v154, v154, v161
	v_max_f32_e32 v161, v174, v157
	v_min_f32_e32 v157, v174, v157
	v_max_f32_e32 v174, v151, v160
	v_min_f32_e32 v151, v151, v160
	v_max_f32_e32 v186, v188, v164
	v_min_f32_e32 v164, v188, v164
	v_max_f32_e32 v188, v184, v167
	v_min_f32_e32 v167, v184, v167
	v_max_f32_e32 v184, v189, v178
	v_min_f32_e32 v178, v189, v178
	v_max_f32_e32 v189, v179, v165
	v_min_f32_e32 v165, v179, v165
	v_max_f32_e32 v179, v180, v182
	v_min_f32_e32 v180, v180, v182
	v_max_f32_e32 v182, v181, v187
	v_min_f32_e32 v181, v181, v187
	v_max_f32_e32 v187, v194, v185
	v_min_f32_e32 v185, v194, v185
	v_max_f32_e32 v194, v166, v183
	v_min_f32_e32 v166, v166, v183
	v_max_f32_e32 v160, v159, v170
	v_min_f32_e32 v159, v159, v170
	v_max_f32_e32 v170, v163, v173
	v_min_f32_e32 v163, v163, v173
	v_max_f32_e32 v173, v171, v161
	v_min_f32_e32 v161, v171, v161
	v_max_f32_e32 v171, v172, v174
	v_min_f32_e32 v172, v172, v174
	v_max_f32_e32 v174, v156, v155
	v_min_f32_e32 v155, v156, v155
	v_max_f32_e32 v156, v152, v154
	v_min_f32_e32 v152, v152, v154
	v_max_f32_e32 v154, v153, v157
	v_min_f32_e32 v153, v153, v157
	v_max_f32_e32 v157, v158, v151
	v_min_f32_e32 v151, v158, v151
	v_max_f32_e32 v183, v186, v179
	v_min_f32_e32 v179, v186, v179
	v_max_f32_e32 v186, v188, v182
	v_min_f32_e32 v182, v188, v182
	v_max_f32_e32 v188, v184, v187
	v_min_f32_e32 v184, v184, v187
	v_max_f32_e32 v187, v189, v194
	v_min_f32_e32 v189, v189, v194
	v_max_f32_e32 v194, v164, v180
	v_min_f32_e32 v164, v164, v180
	v_max_f32_e32 v180, v167, v181
	v_min_f32_e32 v167, v167, v181
	v_max_f32_e32 v181, v178, v185
	v_min_f32_e32 v178, v178, v185
	v_max_f32_e32 v185, v165, v166
	v_min_f32_e32 v165, v165, v166
	v_max_f32_e32 v158, v160, v173
	v_min_f32_e32 v160, v160, v173
	v_max_f32_e32 v173, v170, v171
	v_min_f32_e32 v170, v170, v171
	v_max_f32_e32 v171, v159, v161
	v_min_f32_e32 v159, v159, v161
	v_max_f32_e32 v161, v163, v172
	v_min_f32_e32 v163, v163, v172
	v_max_f32_e32 v172, v174, v154
	v_min_f32_e32 v154, v174, v154
	v_max_f32_e32 v174, v156, v157
	v_min_f32_e32 v156, v156, v157
	v_max_f32_e32 v157, v155, v153
	v_min_f32_e32 v153, v155, v153
	v_max_f32_e32 v155, v152, v151
	v_min_f32_e32 v151, v152, v151
	v_max_f32_e32 v166, v183, v188
	v_min_f32_e32 v183, v183, v188
	v_max_f32_e32 v188, v186, v187
	v_min_f32_e32 v186, v186, v187
	v_max_f32_e32 v187, v179, v184
	v_min_f32_e32 v179, v179, v184
	v_max_f32_e32 v184, v182, v189
	v_min_f32_e32 v182, v182, v189
	v_max_f32_e32 v189, v194, v181
	v_min_f32_e32 v181, v194, v181
	v_max_f32_e32 v194, v180, v185
	v_min_f32_e32 v180, v180, v185
	v_max_f32_e32 v185, v164, v178
	v_min_f32_e32 v164, v164, v178
	v_max_f32_e32 v178, v167, v165
	v_min_f32_e32 v165, v167, v165
	v_min_f32_e32 v152, v158, v173
	v_min_f32_e32 v175, v160, v170
	v_min_f32_e32 v176, v171, v161
	v_min_f32_e32 v177, v159, v163
	v_min_f32_e32 v190, v172, v174
	v_min_f32_e32 v191, v154, v156
	v_min_f32_e32 v192, v157, v155
	v_min_f32_e32 v193, v153, v151
	v_min_f32_e32 v167, v166, v188
	v_min_f32_e32 v195, v183, v186
	v_min_f32_e32 v196, v187, v184
	v_min_f32_e32 v197, v179, v182
	v_min_f32_e32 v198, v189, v194
	v_min_f32_e32 v199, v181, v180
	v_min_f32_e32 v200, v185, v178
	v_min_f32_e32 v201, v164, v165
	v_max3_f32 v158, v158, v173, v201
	v_max3_f32 v152, v152, v164, v165
	v_max3_f32 v160, v160, v170, v200
	v_max3_f32 v164, v175, v185, v178
	v_max3_f32 v161, v171, v161, v199
	v_max3_f32 v165, v176, v181, v180
	v_max3_f32 v159, v159, v163, v198
	v_max3_f32 v163, v177, v189, v194
; __device__ __forceinline__ float shx(float v, int m, int lane) { return __builtin_bit_cast(float, shx_i(__builtin_bit_cast(int, v), m, lane)); }
; __device__ __forceinline__ void ce_desc(float& a, float& b) { const float mx = __builtin_fmaxf(a, b), mn = __builtin_fminf(a, b); a = mx; b = mn; }
; __device__ __forceinline__ void bitonic_merge16_desc(float (&a)[16]) {
; #pragma unroll
;     for (int j = 8; j > 0; j >>= 1)
; #pragma unroll
;         for (int i = 0; i < 16; ++i) { const int l = i ^ j; if (l > i) ce_desc(a[i], a[l]); }
; }
; __device__ __forceinline__ void sort8_desc(float (&a)[8]) {
; #pragma unroll
;     for (int k = 2; k <= 8; k <<= 1)
; #pragma unroll
;         for (int j = k >> 1; j > 0; j >>= 1)
; #pragma unroll
;             for (int i = 0; i < 8; ++i) { const int l = i ^ j; if (l > i) { if ((i & k) == 0 || k == 8) ce_desc(a[i], a[l]); else ce_desc(a[l], a[i]); } }
; }
; __device__ __forceinline__ void xlane_merge16(float (&a)[16], int xm, int lane) {
;     float b[16];
; #pragma unroll
;     for (int i = 0; i < 16; ++i) b[i] = shx(a[15 - i], xm, lane);
; #pragma unroll
;     for (int i = 0; i < 16; ++i) a[i] = __builtin_fmaxf(a[i], b[i]);
;     bitonic_merge16_desc(a);
; }
; __device__ __forceinline__ void ph_topk(const Frame& F, int layer) {
;     ...
;             for (int i = 0; i < 16; ++i) lo[i] = __builtin_fmaxf(lo[i], hi[15 - i]);
;             bitonic_merge16_desc(lo);
;             xlane_merge16(lo, 16, lane); xlane_merge16(lo, 32, lane);
	v_max3_f32 v170, v172, v174, v197
	v_max3_f32 v171, v190, v179, v182
	v_max3_f32 v154, v154, v156, v196
	v_max3_f32 v156, v191, v187, v184
	v_max3_f32 v155, v157, v155, v195
	v_max3_f32 v157, v192, v183, v186
	v_max3_f32 v151, v153, v151, v167
	v_max3_f32 v153, v193, v166, v188
	v_max_f32_e32 v166, v158, v170
	v_min_f32_e32 v158, v158, v170
	v_max_f32_e32 v167, v152, v171
	v_min_f32_e32 v152, v152, v171
	v_max_f32_e32 v170, v160, v154
	v_min_f32_e32 v154, v160, v154
	v_max_f32_e32 v160, v164, v156
	v_min_f32_e32 v156, v164, v156
	v_max_f32_e32 v164, v161, v155
	v_min_f32_e32 v155, v161, v155
	v_max_f32_e32 v161, v165, v157
	v_min_f32_e32 v157, v165, v157
	v_max_f32_e32 v165, v159, v151
	v_min_f32_e32 v151, v159, v151
	v_max_f32_e32 v159, v163, v153
	v_min_f32_e32 v153, v163, v153
	v_min_f32_e32 v123, v127, v123
	v_max_f32_e32 v127, v120, v131
	v_min_f32_e32 v120, v120, v131
	v_max_f32_e32 v131, v122, v119
	v_min_f32_e32 v119, v122, v119
	v_max_f32_e32 v122, v125, v121
	v_min_f32_e32 v121, v125, v121
	v_max_f32_e32 v163, v166, v164
	v_min_f32_e32 v164, v166, v164
	v_max_f32_e32 v166, v167, v161
	v_min_f32_e32 v161, v167, v161
	v_max_f32_e32 v167, v170, v165
	v_min_f32_e32 v165, v170, v165
	v_max_f32_e32 v170, v160, v159
	v_min_f32_e32 v159, v160, v159
	v_max_f32_e32 v160, v158, v155
	v_min_f32_e32 v155, v158, v155
	v_max_f32_e32 v158, v152, v157
	v_min_f32_e32 v152, v152, v157
	v_max_f32_e32 v157, v154, v151
	v_min_f32_e32 v151, v154, v151
	v_max_f32_e32 v154, v156, v153
	v_min_f32_e32 v153, v156, v153
	v_max_f32_e32 v125, v134, v132
	v_min_f32_e32 v132, v134, v132
	v_max_f32_e32 v134, v129, v135
	v_min_f32_e32 v129, v129, v135
	v_max_f32_e32 v135, v126, v133
	v_min_f32_e32 v126, v126, v133
	v_max_f32_e32 v133, v128, v124
	v_min_f32_e32 v124, v128, v124
	v_max_f32_e32 v128, v130, v131
	v_min_f32_e32 v130, v130, v131
	v_max_f32_e32 v131, v127, v122
	v_min_f32_e32 v122, v127, v122
	v_max_f32_e32 v127, v123, v119
	v_min_f32_e32 v119, v123, v119
	v_max_f32_e32 v123, v120, v121
	v_min_f32_e32 v120, v120, v121
	v_max_f32_e32 v156, v163, v167
	v_min_f32_e32 v163, v163, v167
	v_max_f32_e32 v167, v166, v170
	v_min_f32_e32 v166, v166, v170
	v_max_f32_e32 v170, v164, v165
	v_min_f32_e32 v164, v164, v165
	v_max_f32_e32 v165, v161, v159
	v_min_f32_e32 v159, v161, v159
	v_max_f32_e32 v161, v160, v157
	v_min_f32_e32 v157, v160, v157
	v_max_f32_e32 v160, v158, v154
	v_min_f32_e32 v154, v158, v154
	v_max_f32_e32 v158, v155, v151
	v_min_f32_e32 v151, v155, v151
	v_max_f32_e32 v155, v152, v153
	v_min_f32_e32 v152, v152, v153
	v_max_f32_e32 v121, v125, v134
	v_min_f32_e32 v125, v125, v134
	v_max_f32_e32 v134, v132, v129
	v_min_f32_e32 v129, v132, v129
	v_max_f32_e32 v132, v135, v133
	v_min_f32_e32 v133, v135, v133
	v_max_f32_e32 v135, v126, v124
	v_min_f32_e32 v124, v126, v124
	v_max_f32_e32 v126, v128, v131
	v_min_f32_e32 v128, v128, v131
	v_max_f32_e32 v131, v130, v122
	v_min_f32_e32 v122, v130, v122
	v_max_f32_e32 v130, v127, v123
	v_min_f32_e32 v123, v127, v123
	v_max_f32_e32 v127, v119, v120
	v_min_f32_e32 v119, v119, v120
	v_max_f32_e32 v153, v156, v167
	v_min_f32_e32 v156, v156, v167
	v_max_f32_e32 v167, v163, v166
	v_min_f32_e32 v163, v163, v166
	v_max_f32_e32 v166, v170, v165
	v_min_f32_e32 v165, v170, v165
	v_max_f32_e32 v170, v164, v159
	v_min_f32_e32 v159, v164, v159
	v_max_f32_e32 v164, v161, v160
	v_min_f32_e32 v160, v161, v160
	v_max_f32_e32 v161, v157, v154
	v_min_f32_e32 v154, v157, v154
	v_max_f32_e32 v157, v158, v155
	v_min_f32_e32 v155, v158, v155
	v_max_f32_e32 v158, v151, v152
	v_min_f32_e32 v151, v151, v152
	ds_bpermute_b32 v120, v58, v119
	ds_bpermute_b32 v152, v58, v151
	ds_bpermute_b32 v136, v58, v127
	ds_bpermute_b32 v171, v58, v158
	ds_bpermute_b32 v137, v58, v123
	ds_bpermute_b32 v172, v58, v155
	ds_bpermute_b32 v138, v58, v130
	ds_bpermute_b32 v173, v58, v157
	ds_bpermute_b32 v139, v58, v122
	ds_bpermute_b32 v174, v58, v154
	ds_bpermute_b32 v140, v58, v131
	s_waitcnt lgkmcnt(10)
	v_max_f32_e32 v120, v120, v120
	ds_bpermute_b32 v175, v58, v161
	s_waitcnt lgkmcnt(10)
	v_max_f32_e32 v152, v152, v152
	ds_bpermute_b32 v141, v58, v128
	ds_bpermute_b32 v150, v58, v121
	v_max_f32_e32 v120, v121, v120
	s_waitcnt lgkmcnt(11)
	v_max_f32_e32 v121, v136, v136
	ds_bpermute_b32 v176, v58, v160
	ds_bpermute_b32 v185, v58, v153
	v_max_f32_e32 v152, v153, v152
	s_waitcnt lgkmcnt(12)
	v_max_f32_e32 v153, v171, v171
	ds_bpermute_b32 v142, v58, v126
	ds_bpermute_b32 v149, v58, v125
	v_max_f32_e32 v121, v125, v121
	s_waitcnt lgkmcnt(13)
	v_max_f32_e32 v125, v137, v137
	ds_bpermute_b32 v177, v58, v164
	ds_bpermute_b32 v184, v58, v156
	v_max_f32_e32 v153, v156, v153
	s_waitcnt lgkmcnt(14)
	v_max_f32_e32 v156, v172, v172
	ds_bpermute_b32 v143, v58, v124
	ds_bpermute_b32 v148, v58, v134
	v_max_f32_e32 v125, v134, v125
	s_waitcnt lgkmcnt(14)
	v_max_f32_e32 v134, v138, v138
	ds_bpermute_b32 v178, v58, v159
	ds_bpermute_b32 v183, v58, v167
	v_max_f32_e32 v156, v167, v156
	v_max_f32_e32 v167, v173, v173
	ds_bpermute_b32 v144, v58, v135
	ds_bpermute_b32 v147, v58, v129
	v_max_f32_e32 v129, v129, v134
	s_waitcnt lgkmcnt(14)
	v_max_f32_e32 v134, v139, v139
	ds_bpermute_b32 v179, v58, v170
	ds_bpermute_b32 v182, v58, v163
	v_max_f32_e32 v163, v163, v167
	v_max_f32_e32 v167, v174, v174
	ds_bpermute_b32 v145, v58, v133
	ds_bpermute_b32 v146, v58, v132
	v_max_f32_e32 v132, v132, v134
	v_max_f32_e32 v134, v140, v140
	ds_bpermute_b32 v180, v58, v165
	ds_bpermute_b32 v181, v58, v166
	v_max_f32_e32 v166, v166, v167
	v_max_f32_e32 v167, v175, v175
	v_max_f32_e32 v133, v133, v134
	s_waitcnt lgkmcnt(14)
; __device__ __forceinline__ float shx(float v, int m, int lane) { return __builtin_bit_cast(float, shx_i(__builtin_bit_cast(int, v), m, lane)); }
; __device__ __forceinline__ void xlane_merge16(float (&a)[16], int xm, int lane) {
;     float b[16];
; #pragma unroll
;     for (int i = 0; i < 16; ++i) b[i] = shx(a[15 - i], xm, lane);
; #pragma unroll
;     for (int i = 0; i < 16; ++i) a[i] = __builtin_fmaxf(a[i], b[i]);
;     bitonic_merge16_desc(a);
; }
; __device__ __forceinline__ void ph_topk(const Frame& F, int layer) {
;     ...
;             for (int i = 0; i < 16; ++i) lo[i] = __builtin_fmaxf(lo[i], hi[15 - i]);
;             bitonic_merge16_desc(lo);
;             xlane_merge16(lo, 16, lane); xlane_merge16(lo, 32, lane);
	v_max_f32_e32 v134, v141, v141
	v_max_f32_e32 v165, v165, v167
	v_max_f32_e32 v167, v176, v176
	v_max_f32_e32 v134, v135, v134
	v_max_f32_e32 v135, v142, v142
	v_max_f32_e32 v167, v170, v167
	s_waitcnt lgkmcnt(13)
	v_max_f32_e32 v170, v177, v177
	v_max_f32_e32 v124, v124, v135
	s_waitcnt lgkmcnt(11)
	v_max_f32_e32 v135, v143, v143
	v_max_f32_e32 v159, v159, v170
	s_waitcnt lgkmcnt(9)
	v_max_f32_e32 v170, v178, v178
	v_max_f32_e32 v126, v126, v135
	s_waitcnt lgkmcnt(7)
	v_max_f32_e32 v135, v144, v144
	v_max_f32_e32 v164, v164, v170
	s_waitcnt lgkmcnt(5)
	v_max_f32_e32 v170, v179, v179
	v_max_f32_e32 v128, v128, v135
	s_waitcnt lgkmcnt(3)
	v_max_f32_e32 v135, v145, v145
	v_max_f32_e32 v160, v160, v170
	s_waitcnt lgkmcnt(1)
	v_max_f32_e32 v170, v180, v180
	v_max_f32_e32 v131, v131, v135
	v_max_f32_e32 v135, v146, v146
	v_max_f32_e32 v161, v161, v170
	s_waitcnt lgkmcnt(0)
	v_max_f32_e32 v170, v181, v181
	v_max_f32_e32 v122, v122, v135
	v_max_f32_e32 v135, v147, v147
	v_max_f32_e32 v154, v154, v170
	v_max_f32_e32 v170, v182, v182
	v_max_f32_e32 v130, v130, v135
	v_max_f32_e32 v135, v148, v148
	v_max_f32_e32 v157, v157, v170
	v_max_f32_e32 v170, v183, v183
	v_max_f32_e32 v123, v123, v135
	v_max_f32_e32 v135, v149, v149
	v_max_f32_e32 v155, v155, v170
	v_max_f32_e32 v170, v184, v184
	v_max_f32_e32 v127, v127, v135
	v_max_f32_e32 v135, v150, v150
	v_max_f32_e32 v158, v158, v170
	v_max_f32_e32 v170, v185, v185
	v_max_f32_e32 v119, v119, v135
	v_max_f32_e32 v151, v151, v170
	v_max_f32_e32 v135, v120, v126
	v_min_f32_e32 v120, v120, v126
	v_max_f32_e32 v126, v121, v128
	v_min_f32_e32 v121, v121, v128
	v_max_f32_e32 v128, v125, v131
	v_min_f32_e32 v125, v125, v131
	v_max_f32_e32 v131, v129, v122
	v_min_f32_e32 v122, v129, v122
	v_max_f32_e32 v129, v132, v130
	v_min_f32_e32 v130, v132, v130
	v_max_f32_e32 v132, v133, v123
	v_min_f32_e32 v123, v133, v123
	v_max_f32_e32 v133, v134, v127
	v_min_f32_e32 v127, v134, v127
	v_max_f32_e32 v134, v124, v119
	v_min_f32_e32 v119, v124, v119
	v_max_f32_e32 v170, v152, v164
	v_min_f32_e32 v152, v152, v164
	v_max_f32_e32 v164, v153, v160
	v_min_f32_e32 v153, v153, v160
	v_max_f32_e32 v160, v156, v161
	v_min_f32_e32 v156, v156, v161
	v_max_f32_e32 v161, v163, v154
	v_min_f32_e32 v154, v163, v154
	v_max_f32_e32 v163, v166, v157
	v_min_f32_e32 v157, v166, v157
	v_max_f32_e32 v166, v165, v155
	v_min_f32_e32 v155, v165, v155
	v_max_f32_e32 v165, v167, v158
	v_min_f32_e32 v158, v167, v158
	v_max_f32_e32 v167, v159, v151
	v_min_f32_e32 v151, v159, v151
	v_max_f32_e32 v124, v135, v129
	v_min_f32_e32 v129, v135, v129
	v_max_f32_e32 v135, v126, v132
	v_min_f32_e32 v126, v126, v132
	v_max_f32_e32 v132, v128, v133
	v_min_f32_e32 v128, v128, v133
	v_max_f32_e32 v133, v131, v134
	v_min_f32_e32 v131, v131, v134
	v_max_f32_e32 v134, v120, v130
	v_min_f32_e32 v120, v120, v130
	v_max_f32_e32 v130, v121, v123
	v_min_f32_e32 v121, v121, v123
	v_max_f32_e32 v123, v125, v127
	v_min_f32_e32 v125, v125, v127
	v_max_f32_e32 v127, v122, v119
	v_min_f32_e32 v119, v122, v119
	v_max_f32_e32 v159, v170, v163
	v_min_f32_e32 v163, v170, v163
	v_max_f32_e32 v170, v164, v166
	v_min_f32_e32 v164, v164, v166
	v_max_f32_e32 v166, v160, v165
	v_min_f32_e32 v160, v160, v165
	v_max_f32_e32 v165, v161, v167
	v_min_f32_e32 v161, v161, v167
	v_max_f32_e32 v167, v152, v157
	v_min_f32_e32 v152, v152, v157
	v_max_f32_e32 v157, v153, v155
	v_min_f32_e32 v153, v153, v155
	v_max_f32_e32 v155, v156, v158
	v_min_f32_e32 v156, v156, v158
	v_max_f32_e32 v158, v154, v151
	v_min_f32_e32 v151, v154, v151
	v_max_f32_e32 v122, v124, v132
	v_min_f32_e32 v124, v124, v132
	v_max_f32_e32 v132, v135, v133
	v_min_f32_e32 v133, v135, v133
	v_max_f32_e32 v136, v129, v128
	v_min_f32_e32 v128, v129, v128
	v_max_f32_e32 v129, v126, v131
	v_min_f32_e32 v126, v126, v131
	v_max_f32_e32 v138, v134, v123
	v_min_f32_e32 v123, v134, v123
	v_max_f32_e32 v134, v130, v127
	v_min_f32_e32 v130, v130, v127
	v_max_f32_e32 v140, v120, v125
	v_min_f32_e32 v142, v120, v125
	v_max_f32_e32 v120, v121, v119
	v_min_f32_e32 v119, v121, v119
	v_max_f32_e32 v154, v159, v166
	v_min_f32_e32 v159, v159, v166
	v_max_f32_e32 v166, v170, v165
	v_min_f32_e32 v165, v170, v165
	v_max_f32_e32 v170, v163, v160
	v_min_f32_e32 v160, v163, v160
	v_max_f32_e32 v163, v164, v161
	v_min_f32_e32 v164, v164, v161
	v_max_f32_e32 v171, v167, v155
	v_min_f32_e32 v155, v167, v155
	v_max_f32_e32 v167, v157, v158
	v_min_f32_e32 v173, v157, v158
	v_max_f32_e32 v175, v152, v156
	v_min_f32_e32 v177, v152, v156
	v_max_f32_e32 v152, v153, v151
	v_min_f32_e32 v151, v153, v151
	v_max_f32_e32 v141, v122, v132
	v_min_f32_e32 v139, v122, v132
	v_max_f32_e32 v137, v124, v133
	v_min_f32_e32 v135, v124, v133
	v_max_f32_e32 v133, v136, v129
	v_min_f32_e32 v131, v136, v129
	v_max_f32_e32 v129, v128, v126
	v_min_f32_e32 v127, v128, v126
	v_max_f32_e32 v126, v138, v134
	v_min_f32_e32 v125, v138, v134
	v_max_f32_e32 v124, v123, v130
	v_min_f32_e32 v123, v123, v130
	v_max_f32_e32 v122, v140, v120
	v_min_f32_e32 v121, v140, v120
	v_max_f32_e32 v120, v142, v119
	v_min_f32_e32 v119, v142, v119
	v_max_f32_e32 v180, v154, v166
	v_min_f32_e32 v178, v154, v166
	v_max_f32_e32 v176, v159, v165
	v_min_f32_e32 v174, v159, v165
	v_max_f32_e32 v172, v170, v163
	v_min_f32_e32 v170, v170, v163
	v_max_f32_e32 v161, v160, v164
	v_min_f32_e32 v159, v160, v164
	v_max_f32_e32 v158, v171, v167
	v_min_f32_e32 v157, v171, v167
	v_max_f32_e32 v156, v155, v173
	v_min_f32_e32 v155, v155, v173
	v_max_f32_e32 v154, v175, v152
	v_min_f32_e32 v153, v175, v152
	v_max_f32_e32 v152, v177, v151
	v_min_f32_e32 v151, v177, v151
	ds_bpermute_b32 v150, v59, v119
	ds_bpermute_b32 v149, v59, v120
	ds_bpermute_b32 v148, v59, v121
	ds_bpermute_b32 v147, v59, v122
	ds_bpermute_b32 v146, v59, v123
	ds_bpermute_b32 v145, v59, v124
	ds_bpermute_b32 v144, v59, v125
	ds_bpermute_b32 v143, v59, v126
	ds_bpermute_b32 v142, v59, v127
	ds_bpermute_b32 v140, v59, v129
	ds_bpermute_b32 v138, v59, v131
	ds_bpermute_b32 v136, v59, v133
	ds_bpermute_b32 v134, v59, v135
	ds_bpermute_b32 v132, v59, v137
	ds_bpermute_b32 v130, v59, v139
	ds_bpermute_b32 v128, v59, v141
	ds_bpermute_b32 v189, v59, v151
	ds_bpermute_b32 v188, v59, v152
	ds_bpermute_b32 v187, v59, v153
	ds_bpermute_b32 v186, v59, v154
	ds_bpermute_b32 v185, v59, v155
	ds_bpermute_b32 v184, v59, v156
	ds_bpermute_b32 v183, v59, v157
	ds_bpermute_b32 v182, v59, v158
	ds_bpermute_b32 v181, v59, v159
	ds_bpermute_b32 v179, v59, v161
	ds_bpermute_b32 v177, v59, v170
	ds_bpermute_b32 v175, v59, v172
	ds_bpermute_b32 v173, v59, v174
	ds_bpermute_b32 v171, v59, v176
	ds_bpermute_b32 v163, v59, v178
	ds_bpermute_b32 v160, v59, v180
	s_cbranch_vccnz .LBB0_1312
; __device__ __forceinline__ void ph_topk(const Frame& F, int layer) {
;     ...
;         if (item + F.nwg < 1024) { const int itn = item + F.nwg, hdn = itn & 7, tn = (itn >> 3) * 128 + wave * 16 + l15;
; #pragma unroll
;             for (int p = 0; p < 2; ++p)
; #pragma unroll
;                 for (int st = 0; st < 4; ++st) qfa[p][st] = *(const v4u*)(QB + (size_t)tn * 2048 + hdn * 256 + p * 128 + 8 * g + 32 * st); }
	s_add_i32 s16, s20, s21
	s_and_b32 s16, s16, 0xffffff80
	v_add_u32_e32 v2, s16, v56
	v_ashrrev_i32_e32 v3, 31, v2
	v_lshlrev_b64 v[2:3], 12, v[2:3]
	s_and_b32 s16, s22, 0x700
	v_lshl_add_u64 v[2:3], s[8:9], 0, v[2:3]
	s_lshl_b32 s30, s16, 1
	v_lshl_add_u64 v[2:3], v[2:3], 0, s[30:31]
	v_lshl_add_u64 v[30:31], v[2:3], 0, v[0:1]
	global_load_dwordx4 v[2:5], v[30:31], off
	global_load_dwordx4 v[6:9], v[30:31], off offset:64
	global_load_dwordx4 v[10:13], v[30:31], off offset:128
	global_load_dwordx4 v[14:17], v[30:31], off offset:192
	global_load_dwordx4 v[18:21], v[30:31], off offset:256
	global_load_dwordx4 v[22:25], v[30:31], off offset:320
	global_load_dwordx4 v[26:29], v[30:31], off offset:384
	s_nop 0
	global_load_dwordx4 v[30:33], v[30:31], off offset:448
; __device__ __forceinline__ float shx(float v, int m, int lane) { return __builtin_bit_cast(float, shx_i(__builtin_bit_cast(int, v), m, lane)); }
; __device__ __forceinline__ void xlane_merge16(float (&a)[16], int xm, int lane) {
;     float b[16];
; #pragma unroll
;     for (int i = 0; i < 16; ++i) b[i] = shx(a[15 - i], xm, lane);
; #pragma unroll
;     for (int i = 0; i < 16; ++i) a[i] = __builtin_fmaxf(a[i], b[i]);
;     bitonic_merge16_desc(a);
; }
; __device__ __forceinline__ void ph_topk(const Frame& F, int layer) {
;     ...
;             xlane_merge16(lo, 16, lane); xlane_merge16(lo, 32, lane);
; #pragma unroll
;             for (int i = 0; i < 16; ++i) { if (p == 0) v1[i] = lo[i]; else v2[i] = lo[i]; }
;         }
;         if (item + F.nwg < 1024) { const int itn = item + F.nwg, hdn = itn & 7, tn = (itn >> 3) * 128 + wave * 16 + l15;
; #pragma unroll
;             for (int p = 0; p < 2; ++p)
; #pragma unroll
;                 for (int st = 0; st < 4; ++st) qfa[p][st] = *(const v4u*)(QB + (size_t)tn * 2048 + hdn * 256 + p * 128 + 8 * g + 32 * st); }
;         if (g == 0) {
; #pragma unroll
;             for (int i = 0; i < 16; ++i) { ixl[i] = (int)(__builtin_bit_cast(unsigned, v1[i]) & 0x7Fu); ixl[16 + i] = (int)(__builtin_bit_cast(unsigned, v2[i]) & 0x7Fu); }
.LBB0_1312:
	s_waitcnt lgkmcnt(14)
	v_max_f32_e32 v141, v141, v150
	v_max_f32_e32 v139, v139, v149
	v_max_f32_e32 v137, v137, v148
	v_max_f32_e32 v135, v135, v147
	v_max_f32_e32 v133, v133, v146
	v_max_f32_e32 v131, v131, v145
	v_max_f32_e32 v129, v129, v144
	v_max_f32_e32 v127, v127, v143
	v_max_f32_e32 v126, v126, v142
	v_max_f32_e32 v125, v125, v140
	v_max_f32_e32 v124, v124, v138
	v_max_f32_e32 v123, v123, v136
	v_max_f32_e32 v122, v122, v134
	v_max_f32_e32 v121, v121, v132
	v_max_f32_e32 v120, v120, v130
	v_max_f32_e32 v119, v119, v128
	v_max_f32_e32 v128, v141, v126
	v_min_f32_e32 v126, v141, v126
	v_max_f32_e32 v130, v139, v125
	v_min_f32_e32 v125, v139, v125
	v_max_f32_e32 v132, v137, v124
	v_min_f32_e32 v124, v137, v124
	v_max_f32_e32 v134, v135, v123
	v_min_f32_e32 v123, v135, v123
	v_max_f32_e32 v135, v133, v122
	v_min_f32_e32 v122, v133, v122
	v_max_f32_e32 v133, v131, v121
	v_min_f32_e32 v121, v131, v121
	v_max_f32_e32 v131, v129, v120
	v_min_f32_e32 v120, v129, v120
	v_max_f32_e32 v129, v127, v119
	v_min_f32_e32 v119, v127, v119
	v_max_f32_e32 v127, v128, v135
	v_min_f32_e32 v128, v128, v135
	v_max_f32_e32 v135, v130, v133
	v_min_f32_e32 v130, v130, v133
	v_max_f32_e32 v133, v132, v131
	v_min_f32_e32 v131, v132, v131
	v_max_f32_e32 v132, v134, v129
	v_min_f32_e32 v129, v134, v129
	v_max_f32_e32 v134, v126, v122
	v_min_f32_e32 v122, v126, v122
	v_max_f32_e32 v126, v125, v121
	v_min_f32_e32 v121, v125, v121
	v_max_f32_e32 v125, v124, v120
	v_min_f32_e32 v120, v124, v120
	v_max_f32_e32 v124, v123, v119
	v_min_f32_e32 v119, v123, v119
	v_max_f32_e32 v123, v127, v133
	v_min_f32_e32 v127, v127, v133
	v_max_f32_e32 v133, v135, v132
	v_min_f32_e32 v132, v135, v132
	v_max_f32_e32 v135, v128, v131
	v_min_f32_e32 v128, v128, v131
	v_max_f32_e32 v131, v130, v129
	v_min_f32_e32 v129, v130, v129
	v_max_f32_e32 v130, v134, v125
	v_min_f32_e32 v125, v134, v125
	v_max_f32_e32 v134, v126, v124
	v_min_f32_e32 v124, v126, v124
	v_max_f32_e32 v126, v122, v120
	v_max_f32_e32 v137, v121, v119
	v_min_f32_e32 v136, v122, v120
	v_min_f32_e32 v138, v121, v119
	v_max_f32_e32 v122, v123, v133
	v_min_f32_e32 v148, v123, v133
	v_max_f32_e32 v146, v128, v129
	v_min_f32_e32 v147, v128, v129
	v_max_f32_e32 v121, v126, v137
	v_min_f32_e32 v123, v126, v137
	v_max_f32_e32 v126, v189, v189
	v_max_f32_e32 v128, v180, v180
	v_max_f32_e32 v126, v128, v126
	v_max_f32_e32 v128, v188, v188
	v_max_f32_e32 v129, v178, v178
	v_max_f32_e32 v149, v127, v132
	v_min_f32_e32 v150, v127, v132
	v_max_f32_e32 v128, v129, v128
	s_waitcnt lgkmcnt(13)
	v_max_f32_e32 v129, v187, v187
	v_max_f32_e32 v132, v176, v176
	v_max_f32_e32 v129, v132, v129
	s_waitcnt lgkmcnt(12)
	v_max_f32_e32 v132, v186, v186
	v_max_f32_e32 v133, v174, v174
	v_max_f32_e32 v120, v130, v134
	v_min_f32_e32 v127, v130, v134
	v_max_f32_e32 v132, v133, v132
	s_waitcnt lgkmcnt(11)
	v_max_f32_e32 v133, v185, v185
	v_max_f32_e32 v134, v172, v172
	v_max_f32_e32 v119, v135, v131
	v_min_f32_e32 v140, v135, v131
	v_max_f32_e32 v133, v134, v133
	s_waitcnt lgkmcnt(10)
	v_max_f32_e32 v134, v184, v184
	v_max_f32_e32 v135, v170, v170
	v_max_f32_e32 v130, v125, v124
	v_min_f32_e32 v131, v125, v124
	v_max_f32_e32 v124, v136, v138
	v_min_f32_e32 v125, v136, v138
	v_max_f32_e32 v134, v135, v134
	s_waitcnt lgkmcnt(9)
	v_max_f32_e32 v135, v183, v183
	v_max_f32_e32 v136, v161, v161
	v_max_f32_e32 v135, v136, v135
	s_waitcnt lgkmcnt(8)
	v_max_f32_e32 v136, v182, v182
	v_max_f32_e32 v137, v159, v159
	v_max_f32_e32 v136, v137, v136
	s_waitcnt lgkmcnt(7)
	v_max_f32_e32 v137, v181, v181
	v_max_f32_e32 v138, v158, v158
	v_max_f32_e32 v137, v138, v137
	s_waitcnt lgkmcnt(6)
	v_max_f32_e32 v138, v179, v179
	v_max_f32_e32 v139, v157, v157
	v_max_f32_e32 v138, v139, v138
	s_waitcnt lgkmcnt(5)
	v_max_f32_e32 v139, v177, v177
	v_max_f32_e32 v141, v156, v156
	v_max_f32_e32 v139, v141, v139
	s_waitcnt lgkmcnt(4)
	v_max_f32_e32 v141, v175, v175
	v_max_f32_e32 v142, v155, v155
	v_max_f32_e32 v141, v142, v141
	s_waitcnt lgkmcnt(3)
	v_max_f32_e32 v142, v173, v173
	v_max_f32_e32 v143, v154, v154
	v_max_f32_e32 v142, v143, v142
	s_waitcnt lgkmcnt(2)
	v_max_f32_e32 v143, v171, v171
	v_max_f32_e32 v144, v153, v153
	v_max_f32_e32 v143, v144, v143
	s_waitcnt lgkmcnt(1)
	v_max_f32_e32 v144, v163, v163
	v_max_f32_e32 v145, v152, v152
	v_max_f32_e32 v144, v145, v144
	s_waitcnt lgkmcnt(0)
	v_max_f32_e32 v145, v160, v160
	v_max_f32_e32 v145, v151, v145
	v_max_f32_e32 v151, v126, v137
	v_min_f32_e32 v126, v126, v137
	v_max_f32_e32 v137, v128, v138
	v_min_f32_e32 v128, v128, v138
	v_max_f32_e32 v138, v129, v139
	v_min_f32_e32 v129, v129, v139
	v_max_f32_e32 v139, v132, v141
	v_min_f32_e32 v132, v132, v141
	v_max_f32_e32 v141, v133, v142
	v_min_f32_e32 v133, v133, v142
	v_max_f32_e32 v142, v134, v143
	v_min_f32_e32 v134, v134, v143
	v_max_f32_e32 v143, v135, v144
	v_min_f32_e32 v135, v135, v144
	v_max_f32_e32 v144, v136, v145
	v_min_f32_e32 v136, v136, v145
	v_max_f32_e32 v145, v151, v141
	v_min_f32_e32 v141, v151, v141
	v_max_f32_e32 v151, v137, v142
	v_min_f32_e32 v137, v137, v142
	v_max_f32_e32 v142, v138, v143
	v_min_f32_e32 v138, v138, v143
	v_max_f32_e32 v143, v139, v144
	v_min_f32_e32 v139, v139, v144
	v_max_f32_e32 v144, v126, v133
	v_min_f32_e32 v126, v126, v133
	v_max_f32_e32 v133, v128, v134
	v_min_f32_e32 v128, v128, v134
	v_max_f32_e32 v134, v129, v135
	v_min_f32_e32 v129, v129, v135
	v_max_f32_e32 v135, v132, v136
	v_min_f32_e32 v132, v132, v136
	v_max_f32_e32 v136, v145, v142
	v_min_f32_e32 v142, v145, v142
	v_max_f32_e32 v145, v151, v143
	v_min_f32_e32 v143, v151, v143
	v_max_f32_e32 v151, v141, v138
	v_min_f32_e32 v138, v141, v138
	v_max_f32_e32 v141, v137, v139
	v_min_f32_e32 v137, v137, v139
	v_max_f32_e32 v152, v144, v134
	v_min_f32_e32 v134, v144, v134
	v_max_f32_e32 v153, v133, v135
	v_min_f32_e32 v133, v133, v135
	v_max_f32_e32 v154, v126, v129
	v_min_f32_e32 v155, v126, v129
	v_max_f32_e32 v156, v128, v132
	v_min_f32_e32 v132, v128, v132
	v_max_f32_e32 v126, v136, v145
	v_min_f32_e32 v129, v136, v145
	v_max_f32_e32 v128, v142, v143
	v_min_f32_e32 v145, v142, v143
	v_max_f32_e32 v144, v151, v141
	v_min_f32_e32 v143, v151, v141
	v_max_f32_e32 v142, v138, v137
	v_min_f32_e32 v141, v138, v137
	v_max_f32_e32 v139, v152, v153
	v_min_f32_e32 v138, v152, v153
	v_max_f32_e32 v137, v134, v133
	v_min_f32_e32 v136, v134, v133
	v_max_f32_e32 v135, v154, v156
	v_min_f32_e32 v134, v154, v156
	v_max_f32_e32 v133, v155, v132
	v_min_f32_e32 v132, v155, v132
	s_and_saveexec_b64 s[16:17], s[0:1]
	s_cbranch_execnz .LBB0_1317
	s_or_b64 exec, exec, s[16:17]
	v_cmp_lt_i32_e32 vcc, 0, v54
	s_and_saveexec_b64 s[16:17], vcc
	s_cbranch_execnz .LBB0_1318

; __device__ __forceinline__ float sel4(int g, float x0, float x1, float x2, float x3) { return (g == 0) ? x0 : ((g == 1) ? x1 : ((g == 2) ? x2 : x3)); }
; __device__ __forceinline__ void ph_topk(const Frame& F, int layer) {
;     ...
;         float c[16], e[8];
;         {
;             const float s0 = sel4(g, v1[0], v1[1], v1[2], v1[3]), s1 = sel4(g, v1[4], v1[5], v1[6], v1[7]);
;             const float s2 = sel4(g, v1[8], v1[9], v1[10], v1[11]), s3 = sel4(g, v1[12], v1[13], v1[14], v1[15]);
;             const int n0 = (g == 0) ? 16 : ((g == 1) ? 8 : ((g == 2) ? 5 : 4));
; #pragma unroll
;             for (int bq = 0; bq < 16; ++bq) c[bq] = (bq < n0) ? packlow(s0 + v2[bq], (unsigned)((g << 4) | bq), 0xFFu) : NEG;
;             e[0] = packlow(s1 + v2[0], (unsigned)(((4 + g) << 4) | 0), 0xFFu);
;             e[1] = packlow(s1 + v2[1], (unsigned)(((4 + g) << 4) | 1), 0xFFu);
;             e[2] = (g == 0) ? packlow(s1 + v2[2], (unsigned)((4 << 4) | 2), 0xFFu) : NEG;
;             e[3] = packlow(s2 + v2[0], (unsigned)(((8 + g) << 4) | 0), 0xFFu);
;             e[4] = packlow(s3 + v2[0], (unsigned)(((12 + g) << 4) | 0), 0xFFu);
;             e[5] = NEG; e[6] = NEG; e[7] = NEG;
;         }
;         sort8_desc(e);
; #pragma unroll
;         for (int i = 8; i < 16; ++i) c[i] = __builtin_fmaxf(c[i], e[15 - i]);
;         bitonic_merge16_desc(c);
;         xlane_merge16(c, 16, lane); xlane_merge16(c, 32, lane);
.LBB0_1338:
	s_or_b64 exec, exec, s[16:17]
	v_add_f32_e32 v123, v126, v122
	v_add_f32_e32 v124, v129, v122
	v_add_f32_e32 v125, v128, v122
	v_add_f32_e32 v127, v145, v122
	v_add_f32_e32 v130, v144, v122
	v_add_f32_e32 v131, v143, v122
	v_add_f32_e32 v140, v142, v122
	v_add_f32_e32 v141, v141, v122
	v_add_f32_e32 v139, v139, v122
	v_add_f32_e32 v138, v138, v122
	v_add_f32_e32 v137, v137, v122
	v_add_f32_e32 v136, v136, v122
	v_add_f32_e32 v135, v135, v122
	v_add_f32_e32 v134, v134, v122
	v_add_f32_e32 v133, v133, v122
	v_add_f32_e32 v122, v132, v122
	v_add_f32_e32 v132, v126, v119
	v_add_f32_e32 v129, v129, v119
	v_add_f32_e32 v119, v128, v119
	v_and_b32_e32 v119, 0xffffff00, v119
	v_or_b32_e32 v119, 0x42, v119
	v_add_f32_e32 v120, v126, v120
	v_and_or_b32 v132, v132, s65, v107
	v_and_or_b32 v129, v129, s65, v108
	v_cndmask_b32_e64 v119, v211, v119, s[0:1]
	v_and_or_b32 v120, v120, s65, v109
	v_add_f32_e32 v121, v126, v121
	v_and_or_b32 v121, v121, s65, v110
	v_max_f32_e32 v126, v129, v129
	v_max_f32_e32 v128, v132, v132
	v_max_f32_e32 v129, v128, v126
	v_min_f32_e32 v126, v128, v126
	v_max_f32_e32 v128, v120, v119
	v_min_f32_e32 v119, v120, v119
	v_max_f32_e32 v120, v121, v121
	v_max_f32_e32 v121, 0xff61b1e6, v120
	v_min_f32_e32 v132, 0xff61b1e6, v120
	v_max_f32_e32 v142, v129, v119
	v_min_f32_e32 v119, v129, v119
	v_max_f32_e32 v129, v126, v128
	v_min_f32_e32 v126, v126, v128
	v_min_f32_e32 v128, 0xff61b1e6, v121
	v_max_f32_e32 v143, 0xff61b1e6, v132
	s_mov_b32 s16, 0xff61b1e6
	v_max_f32_e32 v144, v142, v129
	v_min_f32_e32 v129, v142, v129
	v_max_f32_e32 v142, v119, v126
	v_min_f32_e32 v119, v119, v126
	v_med3_f32 v120, v120, s16, s16
	v_min_f32_e32 v126, v132, v128
	v_max_f32_e32 v121, v143, v121
	v_and_or_b32 v138, v138, s65, v100
	v_and_or_b32 v137, v137, s65, v101
	v_and_or_b32 v134, v134, s65, v104
	v_and_or_b32 v133, v133, s65, v105
	v_max_f32_e32 v128, v144, v126
	v_min_f32_e32 v126, v144, v126
	v_max_f32_e32 v132, v129, v120
	v_min_f32_e32 v129, v129, v120
	v_max_f32_e32 v143, v142, v120
	v_min_f32_e32 v120, v142, v120
	v_max_f32_e32 v142, v119, v121
	v_min_f32_e32 v119, v119, v121
	v_and_or_b32 v124, v124, s65, v92
	v_and_or_b32 v131, v131, s65, v96
	v_cndmask_b32_e64 v138, v211, v138, s[0:1]
	v_cndmask_b32_e64 v137, v211, v137, s[0:1]
	v_cndmask_b32_e64 v134, v211, v134, s[0:1]
	v_cndmask_b32_e64 v133, v211, v133, s[0:1]
	v_max_f32_e32 v121, v128, v143
	v_min_f32_e32 v128, v128, v143
	v_max_f32_e32 v143, v132, v142
	v_min_f32_e32 v132, v132, v142
	v_max_f32_e32 v142, v126, v120
	v_min_f32_e32 v120, v126, v120
	v_max_f32_e32 v126, v129, v119
	v_min_f32_e32 v119, v129, v119
	v_and_or_b32 v125, v125, s65, v93
	v_cndmask_b32_e64 v131, v211, v131, s[6:7]
	v_and_or_b32 v140, v140, s65, v97
	v_and_or_b32 v139, v139, s65, v99
	v_and_or_b32 v136, v136, s65, v102
	v_and_or_b32 v135, v135, s65, v103
	v_min_f32_e32 v129, v121, v143
	v_min_f32_e32 v144, v128, v132
	v_min_f32_e32 v145, v142, v126
	v_min_f32_e32 v146, v120, v119
	v_max3_f32 v119, v138, v120, v119
	v_max_f32_e32 v120, v137, v137
	v_max3_f32 v128, v134, v128, v132
	v_max_f32_e32 v132, v133, v133
	v_and_or_b32 v127, v127, s65, v94
	v_and_or_b32 v130, v130, s65, v95
	v_cndmask_b32_e64 v140, v211, v140, s[6:7]
	v_and_or_b32 v141, v141, s65, v98
	v_cndmask_b32_e64 v139, v211, v139, s[0:1]
	v_cndmask_b32_e64 v136, v211, v136, s[0:1]
	v_cndmask_b32_e64 v135, v211, v135, s[0:1]
	v_and_or_b32 v122, v122, s65, v106
	v_max_f32_e32 v120, v120, v145
	v_max_f32_e32 v129, v132, v129
	v_max_f32_e32 v132, v124, v119
	v_min_f32_e32 v119, v124, v119
	v_max_f32_e32 v124, v125, v125
	v_and_or_b32 v123, v123, s65, v57
	v_cndmask_b32_e64 v130, v211, v130, s[4:5]
	v_cndmask_b32_e64 v141, v211, v141, s[6:7]
	v_cndmask_b32_e64 v122, v211, v122, s[0:1]
	v_max3_f32 v126, v136, v142, v126
	v_max_f32_e32 v125, v124, v120
	v_min_f32_e32 v120, v124, v120
	v_max_f32_e32 v124, v127, v127
	v_max_f32_e32 v133, v131, v128
	v_min_f32_e32 v128, v131, v128
	v_max_f32_e32 v131, v140, v140
	v_max_f32_e32 v139, v139, v146
	v_max_f32_e32 v135, v135, v144
	v_max3_f32 v121, v122, v121, v143
	v_max_f32_e32 v122, v123, v123
	v_max_f32_e32 v127, v124, v126
	v_min_f32_e32 v124, v124, v126
	v_max_f32_e32 v126, v130, v130
	v_max_f32_e32 v134, v131, v129
	v_min_f32_e32 v129, v131, v129
	v_max_f32_e32 v131, v141, v141
	v_max_f32_e32 v123, v122, v139
	v_min_f32_e32 v122, v122, v139
	v_max_f32_e32 v130, v126, v135
	v_min_f32_e32 v126, v126, v135
	v_max_f32_e32 v135, v131, v121
	v_min_f32_e32 v121, v131, v121
	v_max_f32_e32 v131, v123, v130
	v_min_f32_e32 v123, v123, v130
	v_max_f32_e32 v130, v132, v133
	v_min_f32_e32 v132, v132, v133
	v_max_f32_e32 v133, v125, v134
	v_min_f32_e32 v125, v125, v134
	v_max_f32_e32 v134, v127, v135
	v_min_f32_e32 v127, v127, v135
	v_max_f32_e32 v135, v122, v126
	v_min_f32_e32 v122, v122, v126
	v_max_f32_e32 v126, v119, v128
	v_min_f32_e32 v119, v119, v128
	v_max_f32_e32 v128, v120, v129
	v_min_f32_e32 v120, v120, v129
	v_max_f32_e32 v129, v124, v121
	v_min_f32_e32 v121, v124, v121
	v_max_f32_e32 v124, v131, v133
	v_min_f32_e32 v131, v131, v133
	v_max_f32_e32 v133, v130, v134
	v_min_f32_e32 v130, v130, v134
	v_max_f32_e32 v134, v123, v125
	v_min_f32_e32 v123, v123, v125
	v_max_f32_e32 v125, v132, v127
	v_min_f32_e32 v127, v132, v127
	v_max_f32_e32 v132, v135, v128
	v_min_f32_e32 v128, v135, v128
	v_max_f32_e32 v135, v126, v129
	v_min_f32_e32 v126, v126, v129
	v_max_f32_e32 v129, v122, v120
	v_min_f32_e32 v120, v122, v120
	v_max_f32_e32 v122, v119, v121
	v_min_f32_e32 v119, v119, v121
	v_max_f32_e32 v121, v124, v133
	v_min_f32_e32 v124, v124, v133
	v_max_f32_e32 v133, v131, v130
	v_min_f32_e32 v130, v131, v130
	v_max_f32_e32 v131, v134, v125
	v_min_f32_e32 v125, v134, v125
	v_max_f32_e32 v134, v123, v127
	v_min_f32_e32 v123, v123, v127
	v_max_f32_e32 v127, v132, v135
	v_min_f32_e32 v132, v132, v135
	v_max_f32_e32 v135, v128, v126
	v_min_f32_e32 v126, v128, v126
	v_max_f32_e32 v128, v129, v122
	v_min_f32_e32 v122, v129, v122
	v_max_f32_e32 v129, v120, v119
	v_min_f32_e32 v119, v120, v119
	ds_bpermute_b32 v120, v58, v119
	ds_bpermute_b32 v136, v58, v129
	ds_bpermute_b32 v137, v58, v122
	ds_bpermute_b32 v138, v58, v128
	ds_bpermute_b32 v139, v58, v126
	ds_bpermute_b32 v140, v58, v135
	s_waitcnt lgkmcnt(5)
; __device__ __forceinline__ float shx(float v, int m, int lane) { return __builtin_bit_cast(float, shx_i(__builtin_bit_cast(int, v), m, lane)); }
; __device__ __forceinline__ float sel4(int g, float x0, float x1, float x2, float x3) { return (g == 0) ? x0 : ((g == 1) ? x1 : ((g == 2) ? x2 : x3)); }
; __device__ __forceinline__ void xlane_merge16(float (&a)[16], int xm, int lane) {
;     float b[16];
; #pragma unroll
;     for (int i = 0; i < 16; ++i) b[i] = shx(a[15 - i], xm, lane);
; #pragma unroll
;     for (int i = 0; i < 16; ++i) a[i] = __builtin_fmaxf(a[i], b[i]);
;     bitonic_merge16_desc(a);
; }
; __device__ __forceinline__ void ph_topk(const Frame& F, int layer) {
;     ...
;         xlane_merge16(c, 16, lane); xlane_merge16(c, 32, lane);
;         float r[4], ex[4], esum = 0.f;
; #pragma unroll
;         for (int i = 0; i < 4; ++i) { r[i] = sel4(g, c[i], c[4 + i], c[8 + i], c[12 + i]); ex[i] = __expf(r[i] - c[0]); esum += ex[i]; }
	v_max_f32_e32 v120, v120, v120
	ds_bpermute_b32 v141, v58, v132
	ds_bpermute_b32 v150, v58, v121
	v_max_f32_e32 v120, v121, v120
	s_waitcnt lgkmcnt(6)
	v_max_f32_e32 v121, v136, v136
	ds_bpermute_b32 v142, v58, v127
	ds_bpermute_b32 v149, v58, v124
	v_max_f32_e32 v121, v124, v121
	s_waitcnt lgkmcnt(7)
	v_max_f32_e32 v124, v137, v137
	ds_bpermute_b32 v143, v58, v123
	ds_bpermute_b32 v148, v58, v133
	v_max_f32_e32 v124, v133, v124
	s_waitcnt lgkmcnt(8)
	v_max_f32_e32 v133, v138, v138
	ds_bpermute_b32 v144, v58, v134
	ds_bpermute_b32 v147, v58, v130
	v_max_f32_e32 v130, v130, v133
	s_waitcnt lgkmcnt(9)
	v_max_f32_e32 v133, v139, v139
	ds_bpermute_b32 v145, v58, v125
	ds_bpermute_b32 v146, v58, v131
	v_max_f32_e32 v131, v131, v133
	s_waitcnt lgkmcnt(10)
	v_max_f32_e32 v133, v140, v140
	v_max_f32_e32 v125, v125, v133
	s_waitcnt lgkmcnt(9)
	v_max_f32_e32 v133, v141, v141
	v_max_f32_e32 v133, v134, v133
	s_waitcnt lgkmcnt(7)
	v_max_f32_e32 v134, v142, v142
	v_max_f32_e32 v123, v123, v134
	s_waitcnt lgkmcnt(5)
	v_max_f32_e32 v134, v143, v143
	v_max_f32_e32 v127, v127, v134
	s_waitcnt lgkmcnt(3)
	v_max_f32_e32 v134, v144, v144
	v_max_f32_e32 v132, v132, v134
	s_waitcnt lgkmcnt(1)
	v_max_f32_e32 v134, v145, v145
	v_max_f32_e32 v134, v135, v134
	s_waitcnt lgkmcnt(0)
	v_max_f32_e32 v135, v146, v146
	v_max_f32_e32 v126, v126, v135
	v_max_f32_e32 v135, v147, v147
	v_max_f32_e32 v128, v128, v135
	v_max_f32_e32 v135, v148, v148
	v_max_f32_e32 v122, v122, v135
	v_max_f32_e32 v135, v149, v149
	v_max_f32_e32 v129, v129, v135
	v_max_f32_e32 v135, v150, v150
	v_max_f32_e32 v119, v119, v135
	v_max_f32_e32 v135, v120, v127
	v_min_f32_e32 v120, v120, v127
	v_max_f32_e32 v127, v121, v132
	v_min_f32_e32 v121, v121, v132
	v_max_f32_e32 v132, v124, v134
	v_min_f32_e32 v124, v124, v134
	v_max_f32_e32 v134, v130, v126
	v_min_f32_e32 v126, v130, v126
	v_max_f32_e32 v130, v131, v128
	v_min_f32_e32 v128, v131, v128
	v_max_f32_e32 v131, v125, v122
	v_min_f32_e32 v122, v125, v122
	v_max_f32_e32 v125, v133, v129
	v_min_f32_e32 v129, v133, v129
	v_max_f32_e32 v133, v123, v119
	v_min_f32_e32 v119, v123, v119
	v_max_f32_e32 v123, v135, v130
	v_min_f32_e32 v130, v135, v130
	v_max_f32_e32 v135, v127, v131
	v_min_f32_e32 v127, v127, v131
	v_max_f32_e32 v131, v132, v125
	v_min_f32_e32 v125, v132, v125
	v_max_f32_e32 v132, v134, v133
	v_min_f32_e32 v133, v134, v133
	v_max_f32_e32 v134, v120, v128
	v_min_f32_e32 v120, v120, v128
	v_max_f32_e32 v128, v121, v122
	v_min_f32_e32 v121, v121, v122
	v_max_f32_e32 v122, v124, v129
	v_min_f32_e32 v124, v124, v129
	v_max_f32_e32 v129, v126, v119
	v_min_f32_e32 v119, v126, v119
	v_max_f32_e32 v126, v123, v131
	v_min_f32_e32 v123, v123, v131
	v_max_f32_e32 v131, v135, v132
	v_min_f32_e32 v132, v135, v132
	v_max_f32_e32 v136, v130, v125
	v_min_f32_e32 v125, v130, v125
	v_max_f32_e32 v130, v127, v133
	v_min_f32_e32 v127, v127, v133
	v_max_f32_e32 v138, v134, v122
	v_min_f32_e32 v122, v134, v122
	v_max_f32_e32 v134, v128, v129
	v_min_f32_e32 v128, v128, v129
	v_max_f32_e32 v140, v120, v124
	v_min_f32_e32 v142, v120, v124
	v_max_f32_e32 v120, v121, v119
	v_min_f32_e32 v119, v121, v119
	v_max_f32_e32 v141, v126, v131
	v_min_f32_e32 v139, v126, v131
	v_max_f32_e32 v137, v123, v132
	v_min_f32_e32 v135, v123, v132
	v_max_f32_e32 v133, v136, v130
	v_min_f32_e32 v131, v136, v130
	v_max_f32_e32 v129, v125, v127
	v_min_f32_e32 v127, v125, v127
	v_max_f32_e32 v126, v138, v134
	v_min_f32_e32 v125, v138, v134
	v_max_f32_e32 v124, v122, v128
	v_min_f32_e32 v123, v122, v128
	v_max_f32_e32 v122, v140, v120
	v_min_f32_e32 v121, v140, v120
	v_max_f32_e32 v120, v142, v119
	v_min_f32_e32 v119, v142, v119
	ds_bpermute_b32 v150, v59, v119
	ds_bpermute_b32 v149, v59, v120
	ds_bpermute_b32 v148, v59, v121
	ds_bpermute_b32 v147, v59, v122
	ds_bpermute_b32 v146, v59, v123
	ds_bpermute_b32 v145, v59, v124
	ds_bpermute_b32 v144, v59, v125
	ds_bpermute_b32 v143, v59, v126
	ds_bpermute_b32 v142, v59, v127
	ds_bpermute_b32 v140, v59, v129
	ds_bpermute_b32 v138, v59, v131
	ds_bpermute_b32 v136, v59, v133
	ds_bpermute_b32 v134, v59, v135
	ds_bpermute_b32 v132, v59, v137
	ds_bpermute_b32 v130, v59, v139
	ds_bpermute_b32 v128, v59, v141
	s_waitcnt lgkmcnt(14)
	v_max_f32_e32 v150, v150, v150
	s_waitcnt lgkmcnt(13)
	s_waitcnt lgkmcnt(12)
	s_waitcnt lgkmcnt(11)
	s_waitcnt lgkmcnt(10)
	s_waitcnt lgkmcnt(9)
	s_waitcnt lgkmcnt(8)
	s_waitcnt lgkmcnt(7)
	s_waitcnt lgkmcnt(6)
	s_waitcnt lgkmcnt(5)
	s_waitcnt lgkmcnt(4)
	s_waitcnt lgkmcnt(3)
	s_waitcnt lgkmcnt(2)
	s_waitcnt lgkmcnt(1)
	s_waitcnt lgkmcnt(0)
	v_max_f32_e32 v141, v141, v150
	v_max_f32_e32 v139, v139, v149
	v_max_f32_e32 v137, v137, v148
	v_max_f32_e32 v135, v135, v147
	v_max_f32_e32 v133, v133, v146
	v_max_f32_e32 v131, v131, v145
	v_max_f32_e32 v129, v129, v144
	v_max_f32_e32 v127, v127, v143
	v_max_f32_e32 v126, v126, v142
	v_max_f32_e32 v125, v125, v140
	v_max_f32_e32 v124, v124, v138
	v_max_f32_e32 v123, v123, v136
	v_max_f32_e32 v122, v122, v134
	v_max_f32_e32 v121, v121, v132
	v_max_f32_e32 v120, v120, v130
	v_max_f32_e32 v119, v119, v128
	v_max_f32_e32 v128, v141, v126
	v_min_f32_e32 v126, v141, v126
	v_max_f32_e32 v134, v139, v125
	v_min_f32_e32 v138, v139, v125
	v_max_f32_e32 v136, v137, v124
	v_min_f32_e32 v139, v137, v124
	v_max_f32_e32 v140, v135, v123
	v_min_f32_e32 v141, v135, v123
	v_max_f32_e32 v123, v133, v122
	v_max_f32_e32 v124, v131, v121
	v_min_f32_e32 v121, v131, v121
	v_max_f32_e32 v131, v129, v120
	v_min_f32_e32 v120, v129, v120
	v_max_f32_e32 v129, v127, v119
	v_min_f32_e32 v122, v133, v122
	v_max_f32_e32 v132, v128, v123
	v_max_f32_e32 v130, v134, v124
	v_max_f32_e32 v137, v136, v131
	v_min_f32_e32 v133, v136, v131
	v_max_f32_e32 v136, v140, v129
	v_min_f32_e32 v119, v127, v119
	v_min_f32_e32 v125, v128, v123
	v_max_f32_e32 v128, v126, v122
	v_min_f32_e32 v123, v126, v122
	v_max_f32_e32 v126, v138, v121
	v_min_f32_e32 v122, v138, v121
	v_max_f32_e32 v121, v132, v137
	v_max_f32_e32 v144, v130, v136
	v_min_f32_e32 v124, v134, v124
	v_min_f32_e32 v131, v140, v129
	v_max_f32_e32 v135, v139, v120
	v_min_f32_e32 v129, v139, v120
	v_max_f32_e32 v134, v141, v119
	v_min_f32_e32 v127, v141, v119
	v_max_f32_e32 v120, v121, v144
	v_max_f32_e32 v138, v125, v133
	v_max_f32_e32 v139, v124, v131
	v_max_f32_e32 v141, v128, v135
	v_max_f32_e32 v143, v126, v134
	v_max_f32_e32 v140, v123, v129
	v_max_f32_e32 v142, v122, v127
	v_cmp_lt_i32_e32 vcc, 0, v54
	v_mov_b32_e32 v119, v120
	s_and_saveexec_b64 s[16:17], vcc
	s_cbranch_execz .LBB0_1344
	v_cmp_ne_u32_e32 vcc, 1, v54
	s_and_saveexec_b64 s[18:19], vcc
	s_xor_b64 s[18:19], exec, s[18:19]
	v_max_f32_e32 v119, v142, v142
	v_max_f32_e32 v145, v140, v140
	v_max_f32_e32 v119, v145, v119
	v_max_f32_e32 v145, v143, v143
	v_max_f32_e32 v146, v141, v141
	v_max_f32_e32 v145, v146, v145
	v_cndmask_b32_e64 v119, v119, v145, s[2:3]
	s_andn2_saveexec_b64 s[18:19], s[18:19]
	v_max_f32_e32 v119, v139, v139
	v_max_f32_e32 v145, v138, v138
	v_max_f32_e32 v119, v145, v119
	s_or_b64 exec, exec, s[18:19]
; __device__ __forceinline__ void ce_desc(float& a, float& b) { const float mx = __builtin_fmaxf(a, b), mn = __builtin_fminf(a, b); a = mx; b = mn; }
; __device__ __forceinline__ float sel4(int g, float x0, float x1, float x2, float x3) { return (g == 0) ? x0 : ((g == 1) ? x1 : ((g == 2) ? x2 : x3)); }
; __device__ __forceinline__ void bitonic_merge16_desc(float (&a)[16]) {
; #pragma unroll
;     for (int j = 8; j > 0; j >>= 1)
; #pragma unroll
;         for (int i = 0; i < 16; ++i) { const int l = i ^ j; if (l > i) ce_desc(a[i], a[l]); }
; }
; __device__ __forceinline__ void ph_topk(const Frame& F, int layer) {
;     ...
;         xlane_merge16(c, 16, lane); xlane_merge16(c, 32, lane);
;         float r[4], ex[4], esum = 0.f;
; #pragma unroll
;         for (int i = 0; i < 4; ++i) { r[i] = sel4(g, c[i], c[4 + i], c[8 + i], c[12 + i]); ex[i] = __expf(r[i] - c[0]); esum += ex[i]; }
.LBB0_1344:
	s_or_b64 exec, exec, s[16:17]
	v_min_f32_e32 v121, v121, v144
	v_cmp_lt_i32_e32 vcc, 0, v54
	s_and_saveexec_b64 s[16:17], vcc
	s_cbranch_execz .LBB0_1350
	v_cmp_ne_u32_e32 vcc, 1, v54
	s_and_saveexec_b64 s[18:19], vcc
	s_xor_b64 s[18:19], exec, s[18:19]
	v_max_f32_e32 v121, v143, v143
	v_max_f32_e32 v138, v141, v141
	v_min_f32_e32 v121, v138, v121
	v_max_f32_e32 v138, v142, v142
	v_max_f32_e32 v139, v140, v140
	v_min_f32_e32 v138, v139, v138
	v_cndmask_b32_e64 v121, v138, v121, s[2:3]
	s_andn2_saveexec_b64 s[18:19], s[18:19]
	v_max_f32_e32 v121, v139, v139
	v_min_f32_e32 v121, v138, v121
	s_or_b64 exec, exec, s[18:19]
.LBB0_1350:
	s_or_b64 exec, exec, s[16:17]
	v_min_f32_e32 v136, v130, v136
	v_max_f32_e32 v130, v133, v133
	v_min_f32_e32 v125, v125, v130
	v_max_f32_e32 v130, v131, v131
	v_min_f32_e32 v124, v124, v130
	v_max_f32_e32 v130, v135, v135
	v_min_f32_e32 v128, v128, v130
	v_max_f32_e32 v130, v134, v134
	v_min_f32_e32 v130, v126, v130
	v_max_f32_e32 v126, v129, v129
	v_min_f32_e32 v132, v132, v137
	v_min_f32_e32 v126, v123, v126
	v_max_f32_e32 v123, v127, v127
	v_min_f32_e32 v127, v122, v123
	v_max_f32_e32 v122, v132, v136
	v_cmp_lt_i32_e32 vcc, 0, v54
	s_and_saveexec_b64 s[16:17], vcc
	s_cbranch_execz .LBB0_1356
	v_cmp_ne_u32_e32 vcc, 1, v54
	s_and_saveexec_b64 s[18:19], vcc
	s_xor_b64 s[18:19], exec, s[18:19]
	v_max_f32_e32 v122, v130, v130
	v_max_f32_e32 v123, v128, v128
	v_max_f32_e32 v122, v123, v122
	v_max_f32_e32 v123, v127, v127
	v_max_f32_e32 v129, v126, v126
	v_max_f32_e32 v123, v129, v123
	v_cndmask_b32_e64 v122, v123, v122, s[2:3]
	s_andn2_saveexec_b64 s[18:19], s[18:19]
	v_max_f32_e32 v122, v124, v124
	v_max_f32_e32 v123, v125, v125
	v_max_f32_e32 v122, v123, v122
	s_or_b64 exec, exec, s[18:19]
